# v21 + ln_w/ln_b row loads hoisted to prologue; x row groups 2,3 loaded into fresh registers (no reuse of group-0 regs)
# speedup vs baseline: 1.0034x; 1.0034x over previous
.LBB1_2:
	s_or_b64 exec, exec, s[4:5]
	v_lshrrev_b32_e32 v1, 6, v0
	s_lshl_b32 s3, s2, 8
	v_lshl_or_b32 v128, v1, 5, s3
	v_ashrrev_i32_e32 v129, 31, v128
	v_and_b32_e32 v131, 63, v0
	v_lshlrev_b64 v[126:127], 10, v[128:129]
	v_lshl_add_u64 v[8:9], s[20:21], 0, v[126:127]
	v_lshlrev_b32_e32 v124, 4, v131
	v_lshl_add_u64 v[82:83], v[8:9], 0, v[124:125]
	s_movk_i32 s3, 0x1000
	v_mov_b32_e32 v3, 2
	v_add_co_u32_e64 v8, s[4:5], s3, v82
	v_lshlrev_b32_sdwa v7, v3, v0 dst_sel:DWORD dst_unused:UNUSED_PAD src0_sel:DWORD src1_sel:BYTE_0
	s_nop 0
	v_addc_co_u32_e64 v9, s[4:5], 0, v83, s[4:5]
	global_load_dword v3, v7, s[22:23]
	global_load_dword v4, v7, s[24:25]
	global_load_dword v5, v7, s[30:31]
	global_load_dwordx4 v[238:241], v124, s[22:23]
	global_load_dwordx4 v[242:245], v124, s[24:25]
	global_load_dwordx4 v[78:81], v[82:83], off nt
	global_load_dwordx4 v[74:77], v[82:83], off offset:1024 nt
	global_load_dwordx4 v[70:73], v[82:83], off offset:2048 nt
	global_load_dwordx4 v[66:69], v[82:83], off offset:3072 nt
	global_load_dwordx4 v[62:65], v[8:9], off nt
	global_load_dwordx4 v[58:61], v[8:9], off offset:1024 nt
	global_load_dwordx4 v[54:57], v[8:9], off offset:2048 nt
	global_load_dwordx4 v[50:53], v[8:9], off offset:3072 nt
	v_bfe_u32 v7, v0, 5, 1
	v_and_b32_e32 v129, 31, v0
	v_lshl_or_b32 v7, v1, 2, v7
	v_lshlrev_b32_e32 v8, 8, v7
	v_bitop3_b32 v9, v7, v129, 13 bitop3:0x6c
	v_lshl_or_b32 v8, v9, 3, v8
	v_or_b32_e32 v7, 2, v7
	v_lshlrev_b32_e32 v112, 11, v1
	v_lshlrev_b32_e32 v9, 8, v7
	v_bitop3_b32 v7, v7, v129, 15 bitop3:0x6c
	v_readfirstlane_b32 s3, v112
	v_lshlrev_b32_e32 v122, 1, v8
	v_mov_b32_e32 v123, v125
	v_lshl_or_b32 v7, v7, 3, v9
	v_lshl_add_u64 v[8:9], s[26:27], 0, v[122:123]
	s_mov_b32 m0, s3
	s_nop 0
	global_load_lds_dwordx4 v[8:9], off
	s_addk_i32 s3, 0x400
	v_lshlrev_b32_e32 v106, 1, v7
	v_mov_b32_e32 v107, v125
	s_add_u32 s4, s26, 0x4000
	v_lshl_add_u64 v[8:9], s[26:27], 0, v[106:107]
	s_addc_u32 s5, s27, 0
	s_waitcnt vmcnt(11)
	v_add_f32_e32 v7, v10, v11
	s_mov_b32 m0, s3
	s_nop 0
	global_load_lds_dwordx4 v[8:9], off
	v_or_b32_e32 v113, 0x4000, v112
	v_lshl_add_u64 v[8:9], s[4:5], 0, v[122:123]
	v_add_f32_dpp v7, v7, v7 quad_perm:[1,0,3,2] row_mask:0xf bank_mask:0xf bound_ctrl:1
	v_add_f32_dpp v6, v6, v6 quad_perm:[1,0,3,2] row_mask:0xf bank_mask:0xf bound_ctrl:1
	v_readfirstlane_b32 s3, v113
	s_mov_b32 m0, s3
	s_nop 0
	global_load_lds_dwordx4 v[8:9], off
	v_lshl_add_u64 v[8:9], s[4:5], 0, v[106:107]
	v_add_f32_dpp v7, v7, v7 quad_perm:[2,3,0,1] row_mask:0xf bank_mask:0xf bound_ctrl:1
	v_add_f32_dpp v6, v6, v6 quad_perm:[2,3,0,1] row_mask:0xf bank_mask:0xf bound_ctrl:1
	s_addk_i32 s3, 0x400
	s_mov_b32 m0, s3
	s_nop 0
	global_load_lds_dwordx4 v[8:9], off
	v_mov_b32_e32 v8, v7
	v_mov_b32_e32 v9, v6
	v_lshlrev_b32_e32 v12, 2, v131
	v_mov_b32_dpp v8, v8 row_shl:4 row_mask:0xf bank_mask:0x5
	v_mov_b32_dpp v9, v9 row_shl:4 row_mask:0xf bank_mask:0x5
	v_cmp_eq_u32_e64 s[10:11], 0, v131
	v_mov_b32_dpp v8, v7 row_shr:4 row_mask:0xf bank_mask:0xa
	v_mov_b32_dpp v9, v6 row_shr:4 row_mask:0xf bank_mask:0xa
	v_add_f32_e32 v7, v7, v8
	v_add_f32_e32 v6, v6, v9
	s_nop 0
	v_add_f32_dpp v7, v7, v7 row_ror:8 row_mask:0xf bank_mask:0xf bound_ctrl:1
	v_add_f32_dpp v6, v6, v6 row_ror:8 row_mask:0xf bank_mask:0xf bound_ctrl:1
	v_mov_b32_e32 v8, v7
	v_mov_b32_e32 v9, v6
	s_nop 0
	v_permlane16_swap_b32_e32 v7, v8
	v_permlane16_swap_b32_e32 v6, v9
	v_add_f32_e32 v7, v7, v8
	v_add_f32_e32 v6, v6, v9
	v_mov_b32_e32 v8, v7
	v_mov_b32_e32 v9, v6
	s_nop 0
	v_permlane32_swap_b32_e32 v7, v8
	v_permlane32_swap_b32_e32 v6, v9
	s_and_saveexec_b64 s[4:5], s[10:11]
	s_cbranch_execz .LBB1_4
	v_lshlrev_b32_e32 v13, 2, v1
	v_or_b32_e32 v14, 0x18000, v13
	v_add_f32_e32 v7, v7, v8
	v_or_b32_e32 v13, 0x18020, v13
	v_add_f32_e32 v6, v6, v9
	ds_write_b32 v14, v7
	ds_write_b32 v13, v6

.LBB1_6:
	s_or_b64 exec, exec, s[4:5]
	v_mov_b32_e32 v6, 0x18010
	v_mov_b32_e32 v2, 0x18000
	s_waitcnt lgkmcnt(0)
	s_barrier
	s_waitcnt vmcnt(8)
	ds_read_b128 v[2:5], v2
	ds_read_b128 v[6:9], v6
	s_load_dwordx4 s[36:39], s[0:1], 0x20
	s_movk_i32 s0, 0x2000
	v_lshrrev_b32_e32 v125, 4, v131
	s_waitcnt lgkmcnt(0)
	v_mov_b32_e32 v14, v2
	v_mov_b32_e32 v15, v6
	v_mov_b32_e32 v6, v3
	v_pk_add_f32 v[2:3], v[14:15], v[6:7]
	v_mov_b32_e32 v6, v4
	v_mov_b32_e32 v7, v8
	v_mov_b32_e32 v8, v5
	v_pk_add_f32 v[4:5], v[6:7], v[8:9]
	v_mov_b32_e32 v14, 0x18060
	v_pk_add_f32 v[2:3], v[2:3], v[4:5]
	v_add_co_u32_e32 v42, vcc, s0, v82
	v_add_f32_e32 v2, v2, v3
	v_mul_f32_e32 v132, 0x3a800000, v2
	v_and_b32_e32 v107, 15, v0
	v_mov_b32_e32 v2, 0x18020
	v_mov_b32_e32 v3, 0x18030
	v_lshl_add_u32 v13, v13, 2, v14
	v_pk_add_f32 v[10:11], v[10:11], v[132:133] op_sel_hi:[1,0] neg_lo:[0,1] neg_hi:[0,1]
	v_lshlrev_b32_e32 v85, 13, v1
	v_xor_b32_e32 v114, v125, v0
	v_addc_co_u32_e32 v43, vcc, 0, v83, vcc
	s_movk_i32 s0, 0x3000
	ds_read_b128 v[6:9], v2
	ds_read_b128 v[2:5], v3
	ds_write_b64 v13, v[10:11]
	v_lshl_or_b32 v84, v107, 9, v85
	v_lshlrev_b32_e32 v10, 4, v114
	s_movk_i32 s41, 0xf0
	v_add_co_u32_e32 v44, vcc, s0, v82
	v_lshlrev_b32_e32 v130, 2, v12
	v_and_or_b32 v115, v10, s41, v84
	v_addc_co_u32_e32 v45, vcc, 0, v83, vcc
	global_load_dwordx4 v[34:37], v[42:43], off offset:1024 nt
	global_load_dwordx4 v[30:33], v[42:43], off offset:2048 nt
	global_load_dwordx4 v[26:29], v[42:43], off offset:3072 nt
	global_load_dwordx4 v[38:41], v[44:45], off offset:-4096 nt
	global_load_dwordx4 v[22:25], v[44:45], off nt
	global_load_dwordx4 v[18:21], v[44:45], off offset:1024 nt
	global_load_dwordx4 v[14:17], v[44:45], off offset:2048 nt
	global_load_dwordx4 v[10:13], v[44:45], off offset:3072 nt
	s_waitcnt vmcnt(15)
	v_add_f32_e32 v42, v78, v79
	v_add_f32_e32 v43, v80, v81
	v_add_f32_e32 v42, v42, v43
	s_waitcnt vmcnt(14)
	v_add_f32_e32 v43, v74, v75
	v_add_f32_e32 v44, v76, v77
	v_add_f32_e32 v43, v43, v44
	s_waitcnt vmcnt(13)
	v_add_f32_e32 v44, v70, v71
	v_add_f32_e32 v45, v72, v73
	v_add_f32_e32 v44, v44, v45
	s_waitcnt vmcnt(12)
	v_add_f32_e32 v45, v66, v67
	v_add_f32_e32 v49, v68, v69
	v_add_f32_e32 v45, v45, v49
	s_waitcnt vmcnt(11)
	v_add_f32_e32 v49, v62, v63
	v_add_f32_e32 v86, v64, v65
	v_and_b32_e32 v46, 1, v0
	v_add_f32_e32 v49, v49, v86
	s_waitcnt vmcnt(10)
	v_add_f32_e32 v86, v58, v59
	v_add_f32_e32 v88, v60, v61
	v_add_f32_e32 v86, v86, v88
	s_waitcnt vmcnt(9)
	v_add_f32_e32 v88, v54, v55
	v_add_f32_e32 v89, v56, v57
	v_cmp_eq_u32_e64 s[4:5], 1, v46
	v_add_f32_e32 v88, v88, v89
	s_waitcnt vmcnt(8)
	v_add_f32_e32 v89, v50, v51
	v_add_f32_e32 v90, v52, v53
	v_cndmask_b32_e64 v46, v43, v42, s[4:5]
	v_cndmask_b32_e64 v42, v42, v43, s[4:5]
	v_cndmask_b32_e64 v43, v45, v44, s[4:5]
	v_cndmask_b32_e64 v44, v44, v45, s[4:5]
	v_add_f32_e32 v89, v89, v90
	v_cndmask_b32_e64 v45, v49, v86, s[4:5]
	v_add_f32_dpp v43, v43, v44 quad_perm:[1,0,3,2] row_mask:0xf bank_mask:0xf bound_ctrl:1
	v_cndmask_b32_e64 v44, v86, v49, s[4:5]
	v_and_b32_e32 v47, 2, v0
	v_add_f32_dpp v42, v46, v42 quad_perm:[1,0,3,2] row_mask:0xf bank_mask:0xf bound_ctrl:1
	v_add_f32_dpp v44, v44, v45 quad_perm:[1,0,3,2] row_mask:0xf bank_mask:0xf bound_ctrl:1
	v_cndmask_b32_e64 v45, v89, v88, s[4:5]
	v_cndmask_b32_e64 v46, v88, v89, s[4:5]
	v_cmp_eq_u16_e64 s[6:7], 0, v47
	v_and_b32_e32 v48, 4, v0
	v_add_f32_dpp v45, v45, v46 quad_perm:[1,0,3,2] row_mask:0xf bank_mask:0xf bound_ctrl:1
	v_cndmask_b32_e64 v46, v42, v43, s[6:7]
	v_cndmask_b32_e64 v42, v43, v42, s[6:7]
	v_cndmask_b32_e64 v43, v44, v45, s[6:7]
	v_cndmask_b32_e64 v44, v45, v44, s[6:7]
	v_add_f32_dpp v42, v46, v42 quad_perm:[2,3,0,1] row_mask:0xf bank_mask:0xf bound_ctrl:1
	v_cmp_eq_u16_e64 s[8:9], 0, v48
	v_add_f32_dpp v43, v43, v44 quad_perm:[2,3,0,1] row_mask:0xf bank_mask:0xf bound_ctrl:1
	v_lshlrev_b32_e32 v86, 3, v131
	v_cndmask_b32_e64 v44, v42, v43, s[8:9]
	v_cndmask_b32_e64 v42, v43, v42, s[8:9]
	v_mov_b32_e32 v43, v44
	v_and_b32_e32 v87, 8, v87
	v_mov_b32_e32 v116, 0x3727c5ac
	v_mov_b32_dpp v43, v43 row_shl:4 row_mask:0xf bank_mask:0x5
	v_mov_b32_e32 v117, 0x260
	v_bitop3_b32 v141, v125, v0, 4 bitop3:0x36
	v_mov_b32_dpp v43, v44 row_shr:4 row_mask:0xf bank_mask:0xa
	v_add_f32_e32 v42, v42, v43
	v_bitop3_b32 v142, v125, v0, 8 bitop3:0x36
	v_bitop3_b32 v143, v125, v0, 12 bitop3:0x36
	v_add_f32_dpp v42, v42, v42 row_ror:8 row_mask:0xf bank_mask:0xf bound_ctrl:1
	v_mov_b32_e32 v43, v42
	s_nop 1
	v_permlane16_swap_b32_e32 v42, v43
	v_add_f32_e32 v42, v42, v43
	v_mov_b32_e32 v43, v42
	s_nop 1
	v_permlane32_swap_b32_e32 v42, v43
	v_add_f32_e32 v42, v42, v43
	v_mul_f32_e32 v42, 0x3b800000, v42
	s_mov_b32 s3, 0
	v_readlane_b32 s40, v42, 0
	v_readlane_b32 s42, v42, 1
	v_readlane_b32 s44, v42, 2
	v_readlane_b32 s46, v42, 3
	v_readlane_b32 s48, v42, 4
	v_readlane_b32 s50, v42, 5
	v_readlane_b32 s34, v42, 6
	v_readlane_b32 s0, v42, 7
	v_pk_add_f32 v[90:91], v[78:79], s[40:41] op_sel_hi:[1,0] neg_lo:[0,1] neg_hi:[0,1]
	v_pk_add_f32 v[80:81], v[80:81], s[40:41] op_sel_hi:[1,0] neg_lo:[0,1] neg_hi:[0,1]
	v_and_b32_e32 v78, 0x1f0, v86
	v_pk_add_f32 v[76:77], v[76:77], s[42:43] op_sel_hi:[1,0] neg_lo:[0,1] neg_hi:[0,1]
	v_mul_f32_e32 v88, v81, v81
	v_or3_b32 v140, v85, v78, v87
	v_pk_add_f32 v[78:79], v[74:75], s[42:43] op_sel_hi:[1,0] neg_lo:[0,1] neg_hi:[0,1]
	v_mul_f32_e32 v74, v77, v77
	v_fmac_f32_e32 v88, v80, v80
	v_fmac_f32_e32 v74, v76, v76
	v_fmac_f32_e32 v88, v91, v91
	v_fmac_f32_e32 v74, v79, v79
	v_fmac_f32_e32 v88, v90, v90
	v_fmac_f32_e32 v74, v78, v78
	v_cndmask_b32_e64 v75, v74, v88, s[4:5]
	v_cndmask_b32_e64 v74, v88, v74, s[4:5]
	v_mov_b32_e32 v88, 0x1f0
	v_pk_add_f32 v[72:73], v[72:73], s[44:45] op_sel_hi:[1,0] neg_lo:[0,1] neg_hi:[0,1]
	v_add_f32_dpp v89, v75, v74 quad_perm:[1,0,3,2] row_mask:0xf bank_mask:0xf bound_ctrl:1
	v_bitop3_b32 v74, v86, 16, v88 bitop3:0x6c
	v_or3_b32 v138, v85, v74, v87
	v_pk_add_f32 v[74:75], v[70:71], s[44:45] op_sel_hi:[1,0] neg_lo:[0,1] neg_hi:[0,1]
	v_bitop3_b32 v70, v86, 32, v88 bitop3:0x6c
	v_pk_add_f32 v[68:69], v[68:69], s[46:47] op_sel_hi:[1,0] neg_lo:[0,1] neg_hi:[0,1]
	v_mul_f32_e32 v92, v73, v73
	v_or3_b32 v135, v85, v70, v87
	v_pk_add_f32 v[70:71], v[66:67], s[46:47] op_sel_hi:[1,0] neg_lo:[0,1] neg_hi:[0,1]
	v_mul_f32_e32 v66, v69, v69
	v_fmac_f32_e32 v92, v72, v72
	v_fmac_f32_e32 v66, v68, v68
	v_fmac_f32_e32 v92, v75, v75
	v_fmac_f32_e32 v66, v71, v71
	v_fmac_f32_e32 v92, v74, v74
	v_fmac_f32_e32 v66, v70, v70
	v_cndmask_b32_e64 v67, v66, v92, s[4:5]
	v_cndmask_b32_e64 v66, v92, v66, s[4:5]
	v_pk_add_f32 v[64:65], v[64:65], s[48:49] op_sel_hi:[1,0] neg_lo:[0,1] neg_hi:[0,1]
	v_pk_add_f32 v[60:61], v[60:61], s[50:51] op_sel_hi:[1,0] neg_lo:[0,1] neg_hi:[0,1]
	v_add_f32_dpp v66, v67, v66 quad_perm:[1,0,3,2] row_mask:0xf bank_mask:0xf bound_ctrl:1
	v_cndmask_b32_e64 v67, v89, v66, s[6:7]
	v_cndmask_b32_e64 v66, v66, v89, s[6:7]
	v_mul_f32_e32 v92, v65, v65
	v_fmac_f32_e32 v92, v64, v64
	v_add_f32_dpp v89, v67, v66 quad_perm:[2,3,0,1] row_mask:0xf bank_mask:0xf bound_ctrl:1
	v_bitop3_b32 v66, v86, 48, v88 bitop3:0x6c
	v_or3_b32 v134, v85, v66, v87
	v_pk_add_f32 v[66:67], v[62:63], s[48:49] op_sel_hi:[1,0] neg_lo:[0,1] neg_hi:[0,1]
	v_bitop3_b32 v62, v86, 64, v88 bitop3:0x6c
	v_or3_b32 v120, v85, v62, v87
	v_pk_add_f32 v[62:63], v[58:59], s[50:51] op_sel_hi:[1,0] neg_lo:[0,1] neg_hi:[0,1]
	v_mul_f32_e32 v58, v61, v61
	v_fmac_f32_e32 v58, v60, v60
	v_fmac_f32_e32 v92, v67, v67
	v_fmac_f32_e32 v58, v63, v63
	v_fmac_f32_e32 v92, v66, v66
	v_fmac_f32_e32 v58, v62, v62
	v_cndmask_b32_e64 v59, v58, v92, s[4:5]
	v_cndmask_b32_e64 v58, v92, v58, s[4:5]
	v_pk_add_f32 v[56:57], v[56:57], s[34:35] op_sel_hi:[1,0] neg_lo:[0,1] neg_hi:[0,1]
	s_mov_b32 s25, 0x3e6d3387
	v_add_f32_dpp v92, v59, v58 quad_perm:[1,0,3,2] row_mask:0xf bank_mask:0xf bound_ctrl:1
	v_pk_add_f32 v[58:59], v[54:55], s[34:35] op_sel_hi:[1,0] neg_lo:[0,1] neg_hi:[0,1]
	v_pk_add_f32 v[54:55], v[50:51], s[0:1] op_sel_hi:[1,0] neg_lo:[0,1] neg_hi:[0,1]
	v_pk_add_f32 v[50:51], v[52:53], s[0:1] op_sel_hi:[1,0] neg_lo:[0,1] neg_hi:[0,1]
	v_mul_f32_e32 v93, v57, v57
	v_mul_f32_e32 v52, v51, v51
	v_fmac_f32_e32 v93, v56, v56
	v_fmac_f32_e32 v52, v50, v50
	v_fmac_f32_e32 v93, v59, v59
	v_fmac_f32_e32 v52, v55, v55
	v_fmac_f32_e32 v93, v58, v58
	v_fmac_f32_e32 v52, v54, v54
	v_cndmask_b32_e64 v53, v52, v93, s[4:5]
	v_cndmask_b32_e64 v52, v93, v52, s[4:5]
	s_mov_b32 s35, 0xf800000
	s_movk_i32 s0, 0x50
	v_add_f32_dpp v52, v53, v52 quad_perm:[1,0,3,2] row_mask:0xf bank_mask:0xf bound_ctrl:1
	v_cndmask_b32_e64 v53, v92, v52, s[6:7]
	v_cndmask_b32_e64 v52, v52, v92, s[6:7]
	s_mov_b32 s24, 0xbf3a00e3
	s_mov_b32 s22, 0x3f07dc22
	v_add_f32_dpp v52, v53, v52 quad_perm:[2,3,0,1] row_mask:0xf bank_mask:0xf bound_ctrl:1
	v_cndmask_b32_e64 v53, v89, v52, s[8:9]
	v_cndmask_b32_e64 v52, v52, v89, s[8:9]
	v_mov_b32_e32 v89, v53
	s_mov_b32 s34, 0xbe11a98e
	s_mov_b32 s40, 0x3e027906
	v_mov_b32_dpp v89, v89 row_shl:4 row_mask:0xf bank_mask:0x5
	s_mov_b32 s33, 5
	s_nop 0
	v_mov_b32_dpp v89, v53 row_shr:4 row_mask:0xf bank_mask:0xa
	v_add_f32_e32 v52, v52, v89
	v_bitop3_b32 v89, v86, s0, v88 bitop3:0x6c
	v_or3_b32 v121, v85, v89, v87
	v_add_f32_dpp v52, v52, v52 row_ror:8 row_mask:0xf bank_mask:0xf bound_ctrl:1
	v_mov_b32_e32 v53, v52
	s_nop 1
	v_permlane16_swap_b32_e32 v52, v53
	v_add_f32_e32 v52, v52, v53
	v_mov_b32_e32 v53, v52
	s_nop 1
	v_permlane32_swap_b32_e32 v52, v53
	v_add_f32_e32 v52, v52, v53
	v_fmamk_f32 v52, v52, 0x3b800000, v116
	v_mul_f32_e32 v53, 0x4f800000, v52
	v_cmp_gt_f32_e32 vcc, s35, v52
	s_nop 1
	v_cndmask_b32_e32 v52, v52, v53, vcc
	v_sqrt_f32_e32 v53, v52
	s_nop 0
	v_add_u32_e32 v89, -1, v53
	v_fma_f32 v92, -v89, v53, v52
	v_cmp_ge_f32_e64 s[0:1], 0, v92
	v_add_u32_e32 v92, 1, v53
	s_nop 0
	v_cndmask_b32_e64 v89, v53, v89, s[0:1]
	v_fma_f32 v53, -v92, v53, v52
	v_cmp_lt_f32_e64 s[0:1], 0, v53
	s_nop 1
	v_cndmask_b32_e64 v53, v89, v92, s[0:1]
	v_mul_f32_e32 v89, 0x37800000, v53
	v_cndmask_b32_e32 v53, v53, v89, vcc
	v_cmp_class_f32_e32 vcc, v52, v117
	s_nop 1
	v_cndmask_b32_e32 v52, v53, v52, vcc
	v_div_scale_f32 v53, s[0:1], v52, v52, 1.0
	v_rcp_f32_e32 v89, v53
	s_movk_i32 s0, 0x60
	v_bitop3_b32 v92, v86, s0, v88 bitop3:0x6c
	v_or3_b32 v118, v85, v92, v87
	v_fma_f32 v92, -v53, v89, 1.0
	v_fmac_f32_e32 v89, v92, v89
	v_div_scale_f32 v92, vcc, 1.0, v52, 1.0
	v_mul_f32_e32 v93, v92, v89
	v_fma_f32 v94, -v53, v93, v92
	v_fmac_f32_e32 v93, v94, v89
	v_fma_f32 v53, -v53, v93, v92
	v_div_fmas_f32 v53, v53, v89, v93
	v_div_fixup_f32 v52, v53, v52, 1.0
	s_waitcnt vmcnt(4)
	v_add_f32_e32 v89, v38, v39
	v_readlane_b32 s0, v52, 0
	s_nop 1
	v_pk_mul_f32 v[90:91], s[0:1], v[90:91] op_sel_hi:[0,1]
	s_waitcnt vmcnt(0)
	v_pk_fma_f32 v[92:93], v[90:91], v[238:239], v[242:243]
	v_mov_b64_e32 v[90:91], s[24:25]
	v_fma_f32 v53, |v92|, s25, 1.0
	v_pk_mul_f32 v[98:99], v[92:93], v[92:93]
	v_rcp_f32_e32 v96, v53
	v_mul_f32_e32 v53, 0xbf38aa3b, v98
	v_exp_f32_e32 v98, v53
	v_fma_f32 v53, |v93|, s25, 1.0
	v_rcp_f32_e32 v97, v53
	s_mov_b32 s24, 0x3f35f0e3
	v_pk_mul_f32 v[80:81], s[0:1], v[80:81] op_sel_hi:[0,1]
	v_mul_f32_e32 v53, 0xbf38aa3b, v99
	v_pk_fma_f32 v[100:101], v[96:97], s[22:23], v[90:91] op_sel_hi:[1,0,0]
	v_pk_fma_f32 v[80:81], v[80:81], v[240:241], v[244:245]
	v_pk_fma_f32 v[100:101], v[96:97], v[100:101], s[24:25] op_sel_hi:[1,1,0]
	v_and_b32_e32 v95, 0x7fffffff, v93
	v_pk_fma_f32 v[100:101], v[96:97], v[100:101], s[34:35] op_sel_hi:[1,1,0]
	v_and_b32_e32 v94, 0x7fffffff, v92
	v_pk_fma_f32 v[100:101], v[96:97], v[100:101], s[40:41] op_sel_hi:[1,1,0]
	v_exp_f32_e32 v99, v53
	v_pk_mul_f32 v[96:97], v[96:97], v[100:101]
	v_fma_f32 v53, |v80|, s25, 1.0
	v_pk_mul_f32 v[94:95], v[94:95], v[96:97]
	v_rcp_f32_e32 v96, v53
	v_fma_f32 v53, |v81|, s25, 1.0
	v_rcp_f32_e32 v97, v53
	v_max_f32_e32 v92, 0, v92
	v_max_f32_e32 v93, 0, v93
	v_pk_fma_f32 v[92:93], v[98:99], v[94:95], v[92:93] neg_lo:[1,0,0] neg_hi:[1,0,0]
	v_pk_mul_f32 v[98:99], v[80:81], v[80:81]
	v_pk_fma_f32 v[100:101], v[96:97], s[22:23], v[90:91] op_sel_hi:[1,0,0]
	v_mul_f32_e32 v53, 0xbf38aa3b, v98
	v_exp_f32_e32 v98, v53
	v_pk_fma_f32 v[100:101], v[96:97], v[100:101], s[24:25] op_sel_hi:[1,1,0]
	v_mul_f32_e32 v53, 0xbf38aa3b, v99
	v_pk_fma_f32 v[100:101], v[96:97], v[100:101], s[34:35] op_sel_hi:[1,1,0]
	v_exp_f32_e32 v99, v53
	v_pk_fma_f32 v[100:101], v[96:97], v[100:101], s[40:41] op_sel_hi:[1,1,0]
	v_and_b32_e32 v95, 0x7fffffff, v81
	v_and_b32_e32 v94, 0x7fffffff, v80
	v_pk_mul_f32 v[96:97], v[96:97], v[100:101]
	v_readlane_b32 s0, v52, 1
	v_max_f32_e32 v80, 0, v80
	v_max_f32_e32 v81, 0, v81
	v_pk_mul_f32 v[94:95], v[94:95], v[96:97]
	v_pk_mul_f32 v[78:79], s[0:1], v[78:79] op_sel_hi:[0,1]
	v_pk_fma_f32 v[80:81], v[98:99], v[94:95], v[80:81] neg_lo:[1,0,0] neg_hi:[1,0,0]
	v_pk_fma_f32 v[78:79], v[78:79], v[238:239], v[242:243]
	v_cvt_pk_f16_f32 v92, v92, v93
	v_cvt_pk_f16_f32 v93, v80, v81
	v_fma_f32 v53, |v78|, s25, 1.0
	ds_write_b64 v140, v[92:93] offset:32768
	v_rcp_f32_e32 v92, v53
	v_fma_f32 v53, |v79|, s25, 1.0
	v_rcp_f32_e32 v93, v53
	v_pk_mul_f32 v[94:95], v[78:79], v[78:79]
	v_pk_mul_f32 v[76:77], s[0:1], v[76:77] op_sel_hi:[0,1]
	v_mul_f32_e32 v53, 0xbf38aa3b, v94
	v_pk_fma_f32 v[96:97], v[92:93], s[22:23], v[90:91] op_sel_hi:[1,0,0]
	v_exp_f32_e32 v94, v53
	v_pk_fma_f32 v[96:97], v[92:93], v[96:97], s[24:25] op_sel_hi:[1,1,0]
	v_mul_f32_e32 v53, 0xbf38aa3b, v95
	v_pk_fma_f32 v[96:97], v[92:93], v[96:97], s[34:35] op_sel_hi:[1,1,0]
	v_pk_fma_f32 v[76:77], v[76:77], v[240:241], v[244:245]
	v_pk_fma_f32 v[96:97], v[92:93], v[96:97], s[40:41] op_sel_hi:[1,1,0]
	v_and_b32_e32 v81, 0x7fffffff, v79
	v_and_b32_e32 v80, 0x7fffffff, v78
	v_exp_f32_e32 v95, v53
	v_pk_mul_f32 v[92:93], v[92:93], v[96:97]
	v_fma_f32 v53, |v76|, s25, 1.0
	v_pk_mul_f32 v[80:81], v[80:81], v[92:93]
	v_rcp_f32_e32 v92, v53
	v_fma_f32 v53, |v77|, s25, 1.0
	v_rcp_f32_e32 v93, v53
	v_max_f32_e32 v78, 0, v78
	v_max_f32_e32 v79, 0, v79
	v_pk_fma_f32 v[78:79], v[94:95], v[80:81], v[78:79] neg_lo:[1,0,0] neg_hi:[1,0,0]
	v_pk_mul_f32 v[94:95], v[76:77], v[76:77]
	v_pk_fma_f32 v[96:97], v[92:93], s[22:23], v[90:91] op_sel_hi:[1,0,0]
	v_mul_f32_e32 v53, 0xbf38aa3b, v94
	v_exp_f32_e32 v94, v53
	v_pk_fma_f32 v[96:97], v[92:93], v[96:97], s[24:25] op_sel_hi:[1,1,0]
	v_mul_f32_e32 v53, 0xbf38aa3b, v95
	v_pk_fma_f32 v[96:97], v[92:93], v[96:97], s[34:35] op_sel_hi:[1,1,0]
	v_exp_f32_e32 v95, v53
	v_pk_fma_f32 v[96:97], v[92:93], v[96:97], s[40:41] op_sel_hi:[1,1,0]
	v_and_b32_e32 v81, 0x7fffffff, v77
	v_and_b32_e32 v80, 0x7fffffff, v76
	v_pk_mul_f32 v[92:93], v[92:93], v[96:97]
	v_readlane_b32 s0, v52, 2
	v_max_f32_e32 v76, 0, v76
	v_max_f32_e32 v77, 0, v77
	v_pk_mul_f32 v[80:81], v[80:81], v[92:93]
	v_pk_mul_f32 v[74:75], s[0:1], v[74:75] op_sel_hi:[0,1]
	v_pk_fma_f32 v[76:77], v[94:95], v[80:81], v[76:77] neg_lo:[1,0,0] neg_hi:[1,0,0]
	v_pk_fma_f32 v[74:75], v[74:75], v[238:239], v[242:243]
	v_cvt_pk_f16_f32 v78, v78, v79
	v_cvt_pk_f16_f32 v79, v76, v77
	v_fma_f32 v53, |v74|, s25, 1.0
	ds_write_b64 v138, v[78:79] offset:33280
	v_rcp_f32_e32 v78, v53
	v_fma_f32 v53, |v75|, s25, 1.0
	v_rcp_f32_e32 v79, v53
	v_pk_mul_f32 v[80:81], v[74:75], v[74:75]
	v_pk_mul_f32 v[72:73], s[0:1], v[72:73] op_sel_hi:[0,1]
	v_mul_f32_e32 v53, 0xbf38aa3b, v80
	v_pk_fma_f32 v[92:93], v[78:79], s[22:23], v[90:91] op_sel_hi:[1,0,0]
	v_exp_f32_e32 v80, v53
	v_pk_fma_f32 v[92:93], v[78:79], v[92:93], s[24:25] op_sel_hi:[1,1,0]
	v_mul_f32_e32 v53, 0xbf38aa3b, v81
	v_pk_fma_f32 v[92:93], v[78:79], v[92:93], s[34:35] op_sel_hi:[1,1,0]
	v_pk_fma_f32 v[72:73], v[72:73], v[240:241], v[244:245]
	v_pk_fma_f32 v[92:93], v[78:79], v[92:93], s[40:41] op_sel_hi:[1,1,0]
	v_and_b32_e32 v77, 0x7fffffff, v75
	v_and_b32_e32 v76, 0x7fffffff, v74
	v_exp_f32_e32 v81, v53
	v_pk_mul_f32 v[78:79], v[78:79], v[92:93]
	v_fma_f32 v53, |v72|, s25, 1.0
	v_pk_mul_f32 v[76:77], v[76:77], v[78:79]
	v_rcp_f32_e32 v78, v53
	v_fma_f32 v53, |v73|, s25, 1.0
	v_rcp_f32_e32 v79, v53
	v_max_f32_e32 v74, 0, v74
	v_max_f32_e32 v75, 0, v75
	v_pk_fma_f32 v[74:75], v[80:81], v[76:77], v[74:75] neg_lo:[1,0,0] neg_hi:[1,0,0]
	v_pk_mul_f32 v[80:81], v[72:73], v[72:73]
	v_pk_fma_f32 v[92:93], v[78:79], s[22:23], v[90:91] op_sel_hi:[1,0,0]
	v_mul_f32_e32 v53, 0xbf38aa3b, v80
	v_exp_f32_e32 v80, v53
	v_pk_fma_f32 v[92:93], v[78:79], v[92:93], s[24:25] op_sel_hi:[1,1,0]
	v_mul_f32_e32 v53, 0xbf38aa3b, v81
	v_pk_fma_f32 v[92:93], v[78:79], v[92:93], s[34:35] op_sel_hi:[1,1,0]
	v_exp_f32_e32 v81, v53
	v_pk_fma_f32 v[92:93], v[78:79], v[92:93], s[40:41] op_sel_hi:[1,1,0]
	v_and_b32_e32 v77, 0x7fffffff, v73
	v_and_b32_e32 v76, 0x7fffffff, v72
	v_pk_mul_f32 v[78:79], v[78:79], v[92:93]
	v_readlane_b32 s0, v52, 3
	v_max_f32_e32 v72, 0, v72
	v_max_f32_e32 v73, 0, v73
	v_pk_mul_f32 v[76:77], v[76:77], v[78:79]
	v_pk_mul_f32 v[70:71], s[0:1], v[70:71] op_sel_hi:[0,1]
	v_pk_fma_f32 v[72:73], v[80:81], v[76:77], v[72:73] neg_lo:[1,0,0] neg_hi:[1,0,0]
	v_pk_fma_f32 v[70:71], v[70:71], v[238:239], v[242:243]
	v_cvt_pk_f16_f32 v74, v74, v75
	v_cvt_pk_f16_f32 v75, v72, v73
	v_fma_f32 v53, |v70|, s25, 1.0
	ds_write_b64 v135, v[74:75] offset:33792
	v_rcp_f32_e32 v74, v53
	v_fma_f32 v53, |v71|, s25, 1.0
	v_rcp_f32_e32 v75, v53
	v_pk_mul_f32 v[76:77], v[70:71], v[70:71]
	v_pk_mul_f32 v[68:69], s[0:1], v[68:69] op_sel_hi:[0,1]
	v_mul_f32_e32 v53, 0xbf38aa3b, v76
	v_pk_fma_f32 v[78:79], v[74:75], s[22:23], v[90:91] op_sel_hi:[1,0,0]
	v_exp_f32_e32 v76, v53
	v_pk_fma_f32 v[78:79], v[74:75], v[78:79], s[24:25] op_sel_hi:[1,1,0]
	v_mul_f32_e32 v53, 0xbf38aa3b, v77
	v_pk_fma_f32 v[78:79], v[74:75], v[78:79], s[34:35] op_sel_hi:[1,1,0]
	v_pk_fma_f32 v[68:69], v[68:69], v[240:241], v[244:245]
	v_pk_fma_f32 v[78:79], v[74:75], v[78:79], s[40:41] op_sel_hi:[1,1,0]
	v_and_b32_e32 v73, 0x7fffffff, v71
	v_and_b32_e32 v72, 0x7fffffff, v70
	v_exp_f32_e32 v77, v53
	v_pk_mul_f32 v[74:75], v[74:75], v[78:79]
	v_fma_f32 v53, |v68|, s25, 1.0
	v_pk_mul_f32 v[72:73], v[72:73], v[74:75]
	v_rcp_f32_e32 v74, v53
	v_fma_f32 v53, |v69|, s25, 1.0
	v_rcp_f32_e32 v75, v53
	v_max_f32_e32 v70, 0, v70
	v_max_f32_e32 v71, 0, v71
	v_pk_fma_f32 v[70:71], v[76:77], v[72:73], v[70:71] neg_lo:[1,0,0] neg_hi:[1,0,0]
	v_pk_mul_f32 v[76:77], v[68:69], v[68:69]
	v_pk_fma_f32 v[78:79], v[74:75], s[22:23], v[90:91] op_sel_hi:[1,0,0]
	v_mul_f32_e32 v53, 0xbf38aa3b, v76
	v_exp_f32_e32 v76, v53
	v_pk_fma_f32 v[78:79], v[74:75], v[78:79], s[24:25] op_sel_hi:[1,1,0]
	v_mul_f32_e32 v53, 0xbf38aa3b, v77
	v_pk_fma_f32 v[78:79], v[74:75], v[78:79], s[34:35] op_sel_hi:[1,1,0]
	v_exp_f32_e32 v77, v53
	v_pk_fma_f32 v[78:79], v[74:75], v[78:79], s[40:41] op_sel_hi:[1,1,0]
	v_and_b32_e32 v73, 0x7fffffff, v69
	v_and_b32_e32 v72, 0x7fffffff, v68
	v_pk_mul_f32 v[74:75], v[74:75], v[78:79]
	v_readlane_b32 s0, v52, 4
	v_max_f32_e32 v68, 0, v68
	v_max_f32_e32 v69, 0, v69
	v_pk_mul_f32 v[72:73], v[72:73], v[74:75]
	v_pk_mul_f32 v[66:67], s[0:1], v[66:67] op_sel_hi:[0,1]
	v_pk_fma_f32 v[68:69], v[76:77], v[72:73], v[68:69] neg_lo:[1,0,0] neg_hi:[1,0,0]
	v_pk_fma_f32 v[66:67], v[66:67], v[238:239], v[242:243]
	v_cvt_pk_f16_f32 v70, v70, v71
	v_cvt_pk_f16_f32 v71, v68, v69
	v_fma_f32 v53, |v66|, s25, 1.0
	ds_write_b64 v134, v[70:71] offset:34304
	v_rcp_f32_e32 v70, v53
	v_fma_f32 v53, |v67|, s25, 1.0
	v_rcp_f32_e32 v71, v53
	v_pk_mul_f32 v[72:73], v[66:67], v[66:67]
	v_pk_mul_f32 v[64:65], s[0:1], v[64:65] op_sel_hi:[0,1]
	v_mul_f32_e32 v53, 0xbf38aa3b, v72
	v_pk_fma_f32 v[74:75], v[70:71], s[22:23], v[90:91] op_sel_hi:[1,0,0]
	v_exp_f32_e32 v72, v53
	v_pk_fma_f32 v[74:75], v[70:71], v[74:75], s[24:25] op_sel_hi:[1,1,0]
	v_mul_f32_e32 v53, 0xbf38aa3b, v73
	v_pk_fma_f32 v[74:75], v[70:71], v[74:75], s[34:35] op_sel_hi:[1,1,0]
	v_pk_fma_f32 v[64:65], v[64:65], v[240:241], v[244:245]
	v_pk_fma_f32 v[74:75], v[70:71], v[74:75], s[40:41] op_sel_hi:[1,1,0]
	v_and_b32_e32 v69, 0x7fffffff, v67
	v_and_b32_e32 v68, 0x7fffffff, v66
	v_exp_f32_e32 v73, v53
	v_pk_mul_f32 v[70:71], v[70:71], v[74:75]
	v_fma_f32 v53, |v64|, s25, 1.0
	v_pk_mul_f32 v[68:69], v[68:69], v[70:71]
	v_rcp_f32_e32 v70, v53
	v_fma_f32 v53, |v65|, s25, 1.0
	v_rcp_f32_e32 v71, v53
	v_max_f32_e32 v66, 0, v66
	v_max_f32_e32 v67, 0, v67
	v_pk_fma_f32 v[66:67], v[72:73], v[68:69], v[66:67] neg_lo:[1,0,0] neg_hi:[1,0,0]
	v_pk_mul_f32 v[72:73], v[64:65], v[64:65]
	v_pk_fma_f32 v[74:75], v[70:71], s[22:23], v[90:91] op_sel_hi:[1,0,0]
	v_mul_f32_e32 v53, 0xbf38aa3b, v72
	v_exp_f32_e32 v72, v53
	v_pk_fma_f32 v[74:75], v[70:71], v[74:75], s[24:25] op_sel_hi:[1,1,0]
	v_mul_f32_e32 v53, 0xbf38aa3b, v73
	v_pk_fma_f32 v[74:75], v[70:71], v[74:75], s[34:35] op_sel_hi:[1,1,0]
	v_exp_f32_e32 v73, v53
	v_pk_fma_f32 v[74:75], v[70:71], v[74:75], s[40:41] op_sel_hi:[1,1,0]
	v_and_b32_e32 v69, 0x7fffffff, v65
	v_and_b32_e32 v68, 0x7fffffff, v64
	v_pk_mul_f32 v[70:71], v[70:71], v[74:75]
	v_readlane_b32 s0, v52, 5
	v_max_f32_e32 v64, 0, v64
	v_max_f32_e32 v65, 0, v65
	v_pk_mul_f32 v[68:69], v[68:69], v[70:71]
	v_pk_mul_f32 v[62:63], s[0:1], v[62:63] op_sel_hi:[0,1]
	v_pk_fma_f32 v[64:65], v[72:73], v[68:69], v[64:65] neg_lo:[1,0,0] neg_hi:[1,0,0]
	v_pk_fma_f32 v[62:63], v[62:63], v[238:239], v[242:243]
	v_cvt_pk_f16_f32 v66, v66, v67
	v_cvt_pk_f16_f32 v67, v64, v65
	v_fma_f32 v53, |v62|, s25, 1.0
	ds_write_b64 v120, v[66:67] offset:34816
	v_rcp_f32_e32 v66, v53
	v_fma_f32 v53, |v63|, s25, 1.0
	v_rcp_f32_e32 v67, v53
	v_pk_mul_f32 v[68:69], v[62:63], v[62:63]
	v_pk_mul_f32 v[60:61], s[0:1], v[60:61] op_sel_hi:[0,1]
	v_mul_f32_e32 v53, 0xbf38aa3b, v68
	v_pk_fma_f32 v[70:71], v[66:67], s[22:23], v[90:91] op_sel_hi:[1,0,0]
	v_exp_f32_e32 v68, v53
	v_pk_fma_f32 v[70:71], v[66:67], v[70:71], s[24:25] op_sel_hi:[1,1,0]
	v_mul_f32_e32 v53, 0xbf38aa3b, v69
	v_pk_fma_f32 v[70:71], v[66:67], v[70:71], s[34:35] op_sel_hi:[1,1,0]
	v_pk_fma_f32 v[60:61], v[60:61], v[240:241], v[244:245]
	v_pk_fma_f32 v[70:71], v[66:67], v[70:71], s[40:41] op_sel_hi:[1,1,0]
	v_and_b32_e32 v65, 0x7fffffff, v63
	v_and_b32_e32 v64, 0x7fffffff, v62
	v_exp_f32_e32 v69, v53
	v_pk_mul_f32 v[66:67], v[66:67], v[70:71]
	v_fma_f32 v53, |v60|, s25, 1.0
	v_pk_mul_f32 v[64:65], v[64:65], v[66:67]
	v_rcp_f32_e32 v66, v53
	v_fma_f32 v53, |v61|, s25, 1.0
	v_rcp_f32_e32 v67, v53
	v_max_f32_e32 v62, 0, v62
	v_max_f32_e32 v63, 0, v63
	v_pk_fma_f32 v[62:63], v[68:69], v[64:65], v[62:63] neg_lo:[1,0,0] neg_hi:[1,0,0]
	v_pk_mul_f32 v[68:69], v[60:61], v[60:61]
	v_pk_fma_f32 v[70:71], v[66:67], s[22:23], v[90:91] op_sel_hi:[1,0,0]
	v_mul_f32_e32 v53, 0xbf38aa3b, v68
	v_exp_f32_e32 v68, v53
	v_pk_fma_f32 v[70:71], v[66:67], v[70:71], s[24:25] op_sel_hi:[1,1,0]
	v_mul_f32_e32 v53, 0xbf38aa3b, v69
	v_pk_fma_f32 v[70:71], v[66:67], v[70:71], s[34:35] op_sel_hi:[1,1,0]
	v_exp_f32_e32 v69, v53
	v_pk_fma_f32 v[70:71], v[66:67], v[70:71], s[40:41] op_sel_hi:[1,1,0]
	v_and_b32_e32 v65, 0x7fffffff, v61
	v_and_b32_e32 v64, 0x7fffffff, v60
	v_pk_mul_f32 v[66:67], v[66:67], v[70:71]
	v_readlane_b32 s0, v52, 6
	v_max_f32_e32 v60, 0, v60
	v_max_f32_e32 v61, 0, v61
	v_pk_mul_f32 v[64:65], v[64:65], v[66:67]
	v_pk_mul_f32 v[58:59], s[0:1], v[58:59] op_sel_hi:[0,1]
	v_pk_fma_f32 v[60:61], v[68:69], v[64:65], v[60:61] neg_lo:[1,0,0] neg_hi:[1,0,0]
	v_pk_fma_f32 v[58:59], v[58:59], v[238:239], v[242:243]
	v_cvt_pk_f16_f32 v62, v62, v63
	v_cvt_pk_f16_f32 v63, v60, v61
	v_fma_f32 v53, |v58|, s25, 1.0
	ds_write_b64 v121, v[62:63] offset:35328
	v_rcp_f32_e32 v62, v53
	v_fma_f32 v53, |v59|, s25, 1.0
	v_rcp_f32_e32 v63, v53
	v_pk_mul_f32 v[64:65], v[58:59], v[58:59]
	v_pk_mul_f32 v[56:57], s[0:1], v[56:57] op_sel_hi:[0,1]
	v_mul_f32_e32 v53, 0xbf38aa3b, v64
	v_pk_fma_f32 v[66:67], v[62:63], s[22:23], v[90:91] op_sel_hi:[1,0,0]
	v_exp_f32_e32 v64, v53
	v_pk_fma_f32 v[66:67], v[62:63], v[66:67], s[24:25] op_sel_hi:[1,1,0]
	v_mul_f32_e32 v53, 0xbf38aa3b, v65
	v_pk_fma_f32 v[66:67], v[62:63], v[66:67], s[34:35] op_sel_hi:[1,1,0]
	v_pk_fma_f32 v[56:57], v[56:57], v[240:241], v[244:245]
	v_pk_fma_f32 v[66:67], v[62:63], v[66:67], s[40:41] op_sel_hi:[1,1,0]
	v_and_b32_e32 v61, 0x7fffffff, v59
	v_and_b32_e32 v60, 0x7fffffff, v58
	v_exp_f32_e32 v65, v53
	v_pk_mul_f32 v[62:63], v[62:63], v[66:67]
	v_fma_f32 v53, |v56|, s25, 1.0
	v_pk_mul_f32 v[60:61], v[60:61], v[62:63]
	v_rcp_f32_e32 v62, v53
	v_fma_f32 v53, |v57|, s25, 1.0
	v_rcp_f32_e32 v63, v53
	v_max_f32_e32 v58, 0, v58
	v_max_f32_e32 v59, 0, v59
	v_pk_fma_f32 v[58:59], v[64:65], v[60:61], v[58:59] neg_lo:[1,0,0] neg_hi:[1,0,0]
	v_pk_mul_f32 v[64:65], v[56:57], v[56:57]
	v_pk_fma_f32 v[66:67], v[62:63], s[22:23], v[90:91] op_sel_hi:[1,0,0]
	v_mul_f32_e32 v53, 0xbf38aa3b, v64
	v_exp_f32_e32 v64, v53
	v_pk_fma_f32 v[66:67], v[62:63], v[66:67], s[24:25] op_sel_hi:[1,1,0]
	v_mul_f32_e32 v53, 0xbf38aa3b, v65
	v_pk_fma_f32 v[66:67], v[62:63], v[66:67], s[34:35] op_sel_hi:[1,1,0]
	v_exp_f32_e32 v65, v53
	v_pk_fma_f32 v[66:67], v[62:63], v[66:67], s[40:41] op_sel_hi:[1,1,0]
	v_and_b32_e32 v61, 0x7fffffff, v57
	v_and_b32_e32 v60, 0x7fffffff, v56
	v_pk_mul_f32 v[62:63], v[62:63], v[66:67]
	v_readlane_b32 s0, v52, 7
	v_max_f32_e32 v56, 0, v56
	v_max_f32_e32 v57, 0, v57
	v_pk_mul_f32 v[60:61], v[60:61], v[62:63]
	v_pk_mul_f32 v[52:53], s[0:1], v[54:55] op_sel_hi:[0,1]
	v_pk_fma_f32 v[56:57], v[64:65], v[60:61], v[56:57] neg_lo:[1,0,0] neg_hi:[1,0,0]
	v_pk_fma_f32 v[52:53], v[52:53], v[238:239], v[242:243]
	v_cvt_pk_f16_f32 v58, v58, v59
	v_cvt_pk_f16_f32 v59, v56, v57
	v_fma_f32 v56, |v52|, s25, 1.0
	v_fma_f32 v57, |v53|, s25, 1.0
	v_rcp_f32_e32 v56, v56
	v_rcp_f32_e32 v57, v57
	ds_write_b64 v118, v[58:59] offset:35840
	v_pk_mul_f32 v[58:59], v[52:53], v[52:53]
	v_and_b32_e32 v55, 0x7fffffff, v53
	v_pk_fma_f32 v[60:61], v[56:57], s[22:23], v[90:91] op_sel_hi:[1,0,0]
	v_mul_f32_e32 v58, 0xbf38aa3b, v58
	v_pk_fma_f32 v[60:61], v[56:57], v[60:61], s[24:25] op_sel_hi:[1,1,0]
	v_mul_f32_e32 v59, 0xbf38aa3b, v59
	v_exp_f32_e32 v58, v58
	v_pk_fma_f32 v[60:61], v[56:57], v[60:61], s[34:35] op_sel_hi:[1,1,0]
	v_exp_f32_e32 v59, v59
	v_pk_fma_f32 v[60:61], v[56:57], v[60:61], s[40:41] op_sel_hi:[1,1,0]
	v_and_b32_e32 v54, 0x7fffffff, v52
	v_pk_mul_f32 v[56:57], v[56:57], v[60:61]
	v_max_f32_e32 v52, 0, v52
	v_max_f32_e32 v53, 0, v53
	v_pk_mul_f32 v[54:55], v[54:55], v[56:57]
	v_pk_mul_f32 v[50:51], s[0:1], v[50:51] op_sel_hi:[0,1]
	v_pk_fma_f32 v[52:53], v[58:59], v[54:55], v[52:53] neg_lo:[1,0,0] neg_hi:[1,0,0]
	v_pk_fma_f32 v[50:51], v[50:51], v[240:241], v[244:245]
	v_cvt_pk_f16_f32 v52, v52, v53
	v_fma_f32 v53, |v50|, s25, 1.0
	v_rcp_f32_e32 v56, v53
	v_fma_f32 v53, |v51|, s25, 1.0
	v_rcp_f32_e32 v57, v53
	v_pk_mul_f32 v[58:59], v[50:51], v[50:51]
	v_and_b32_e32 v55, 0x7fffffff, v51
	v_mul_f32_e32 v53, 0xbf38aa3b, v58
	v_pk_fma_f32 v[60:61], v[56:57], s[22:23], v[90:91] op_sel_hi:[1,0,0]
	v_exp_f32_e32 v58, v53
	v_pk_fma_f32 v[60:61], v[56:57], v[60:61], s[24:25] op_sel_hi:[1,1,0]
	v_mul_f32_e32 v53, 0xbf38aa3b, v59
	v_pk_fma_f32 v[60:61], v[56:57], v[60:61], s[34:35] op_sel_hi:[1,1,0]
	v_exp_f32_e32 v59, v53
	v_pk_fma_f32 v[60:61], v[56:57], v[60:61], s[40:41] op_sel_hi:[1,1,0]
	v_and_b32_e32 v54, 0x7fffffff, v50
	v_pk_mul_f32 v[56:57], v[56:57], v[60:61]
	v_max_f32_e32 v50, 0, v50
	v_max_f32_e32 v51, 0, v51
	v_pk_mul_f32 v[54:55], v[54:55], v[56:57]
	s_movk_i32 s0, 0x70
	v_pk_fma_f32 v[50:51], v[58:59], v[54:55], v[50:51] neg_lo:[1,0,0] neg_hi:[1,0,0]
	v_add_f32_e32 v96, v24, v25
	v_cvt_pk_f16_f32 v53, v50, v51
	v_bitop3_b32 v50, v86, s0, v88 bitop3:0x6c
	s_movk_i32 s0, 0x4000
	v_add_co_u32_e32 v92, vcc, s0, v82
	s_movk_i32 s0, 0x5000
	s_nop 0
	v_addc_co_u32_e32 v93, vcc, 0, v83, vcc
	v_or3_b32 v144, v85, v50, v87
	v_add_co_u32_e32 v94, vcc, s0, v82
	ds_write_b64 v144, v[52:53] offset:36352
	s_nop 0
	v_addc_co_u32_e32 v95, vcc, 0, v83, vcc
	s_movk_i32 s56, 0x5000
	v_add_co_u32_e64 v234, s[58:59], s56, v82
	s_nop 1
	v_addc_co_u32_e64 v235, s[58:59], 0, v83, s[58:59]
	global_load_dwordx4 v[170:173], v[234:235], off offset:-4096 nt
	global_load_dwordx4 v[174:177], v[234:235], off offset:-3072 nt
	global_load_dwordx4 v[178:181], v[234:235], off offset:-2048 nt
	global_load_dwordx4 v[182:185], v[234:235], off offset:-1024 nt
	global_load_dwordx4 v[186:189], v[234:235], off nt
	global_load_dwordx4 v[190:193], v[234:235], off offset:1024 nt
	global_load_dwordx4 v[194:197], v[234:235], off offset:2048 nt
	global_load_dwordx4 v[198:201], v[234:235], off offset:3072 nt
	v_add_f32_e32 v92, v40, v41
	v_add_f32_e32 v89, v89, v92
	v_add_f32_e32 v92, v34, v35
	v_add_f32_e32 v93, v36, v37
	v_add_f32_e32 v92, v92, v93
	v_add_f32_e32 v93, v30, v31
	v_add_f32_e32 v94, v32, v33
	v_add_f32_e32 v93, v93, v94
	v_add_f32_e32 v94, v26, v27
	v_add_f32_e32 v95, v28, v29
	v_add_f32_e32 v94, v94, v95
	v_add_f32_e32 v95, v22, v23
	v_add_f32_e32 v95, v95, v96
	v_add_f32_e32 v96, v18, v19
	v_add_f32_e32 v97, v20, v21
	v_add_f32_e32 v96, v96, v97
	v_add_f32_e32 v97, v14, v15
	v_add_f32_e32 v98, v16, v17
	v_add_f32_e32 v97, v97, v98
	v_add_f32_e32 v98, v10, v11
	v_add_f32_e32 v99, v12, v13
	v_add_f32_e32 v98, v98, v99
	v_cndmask_b32_e64 v99, v92, v89, s[4:5]
	v_cndmask_b32_e64 v89, v89, v92, s[4:5]
	v_cndmask_b32_e64 v92, v94, v93, s[4:5]
	v_cndmask_b32_e64 v93, v93, v94, s[4:5]
	v_cndmask_b32_e64 v94, v95, v96, s[4:5]
	v_add_f32_dpp v89, v99, v89 quad_perm:[1,0,3,2] row_mask:0xf bank_mask:0xf bound_ctrl:1
	v_add_f32_dpp v92, v92, v93 quad_perm:[1,0,3,2] row_mask:0xf bank_mask:0xf bound_ctrl:1
	v_cndmask_b32_e64 v93, v96, v95, s[4:5]
	v_cndmask_b32_e64 v95, v97, v98, s[4:5]
	s_movk_i32 s1, 0x80
	v_add_f32_dpp v93, v93, v94 quad_perm:[1,0,3,2] row_mask:0xf bank_mask:0xf bound_ctrl:1
	v_cndmask_b32_e64 v94, v98, v97, s[4:5]
	s_movk_i32 s23, 0x90
	s_nop 0
	v_add_f32_dpp v94, v94, v95 quad_perm:[1,0,3,2] row_mask:0xf bank_mask:0xf bound_ctrl:1
	v_cndmask_b32_e64 v95, v89, v92, s[6:7]
	v_cndmask_b32_e64 v89, v92, v89, s[6:7]
	v_cndmask_b32_e64 v92, v93, v94, s[6:7]
	v_cndmask_b32_e64 v93, v94, v93, s[6:7]
	v_add_f32_dpp v89, v95, v89 quad_perm:[2,3,0,1] row_mask:0xf bank_mask:0xf bound_ctrl:1
	s_nop 0
	v_add_f32_dpp v92, v92, v93 quad_perm:[2,3,0,1] row_mask:0xf bank_mask:0xf bound_ctrl:1
	v_cndmask_b32_e64 v93, v89, v92, s[8:9]
	v_cndmask_b32_e64 v89, v92, v89, s[8:9]
	v_mov_b32_e32 v92, v93
	s_nop 1
	v_mov_b32_dpp v92, v92 row_shl:4 row_mask:0xf bank_mask:0x5
	s_nop 1
	v_mov_b32_dpp v92, v93 row_shr:4 row_mask:0xf bank_mask:0xa
	v_add_f32_e32 v89, v89, v92
	s_nop 1
	v_add_f32_dpp v89, v89, v89 row_ror:8 row_mask:0xf bank_mask:0xf bound_ctrl:1
	v_mov_b32_e32 v92, v89
	s_nop 1
	v_permlane16_swap_b32_e32 v89, v92
	v_add_f32_e32 v89, v89, v92
	v_mov_b32_e32 v92, v89
	s_nop 1
	v_permlane32_swap_b32_e32 v89, v92
	v_add_f32_e32 v89, v89, v92
	v_mul_f32_e32 v89, 0x3b800000, v89
	v_bitop3_b32 v92, v86, s1, v88 bitop3:0x6c
	v_readlane_b32 s44, v89, 0
	v_readlane_b32 s46, v89, 1
	v_readlane_b32 s48, v89, 2
	v_pk_add_f32 v[40:41], v[40:41], s[44:45] op_sel_hi:[1,0] neg_lo:[0,1] neg_hi:[0,1]
	v_pk_add_f32 v[36:37], v[36:37], s[46:47] op_sel_hi:[1,0] neg_lo:[0,1] neg_hi:[0,1]
	v_readlane_b32 s50, v89, 3
	v_readlane_b32 s52, v89, 4
	v_readlane_b32 s54, v89, 5
	v_readlane_b32 s42, v89, 6
	v_readlane_b32 s0, v89, 7
	v_mul_f32_e32 v89, v41, v41
	v_or3_b32 v145, v85, v92, v87
	v_pk_add_f32 v[92:93], v[34:35], s[46:47] op_sel_hi:[1,0] neg_lo:[0,1] neg_hi:[0,1]
	v_mul_f32_e32 v34, v37, v37
	v_pk_add_f32 v[38:39], v[38:39], s[44:45] op_sel_hi:[1,0] neg_lo:[0,1] neg_hi:[0,1]
	v_fmac_f32_e32 v89, v40, v40
	v_fmac_f32_e32 v34, v36, v36
	v_fmac_f32_e32 v89, v39, v39
	v_fmac_f32_e32 v34, v93, v93
	v_fmac_f32_e32 v89, v38, v38
	v_fmac_f32_e32 v34, v92, v92
	v_cndmask_b32_e64 v35, v34, v89, s[4:5]
	v_cndmask_b32_e64 v34, v89, v34, s[4:5]
	s_movk_i32 s1, 0xa0
	v_pk_add_f32 v[32:33], v[32:33], s[48:49] op_sel_hi:[1,0] neg_lo:[0,1] neg_hi:[0,1]
	v_add_f32_dpp v89, v35, v34 quad_perm:[1,0,3,2] row_mask:0xf bank_mask:0xf bound_ctrl:1
	v_bitop3_b32 v34, v86, s23, v88 bitop3:0x6c
	v_or3_b32 v139, v85, v34, v87
	v_pk_add_f32 v[34:35], v[30:31], s[48:49] op_sel_hi:[1,0] neg_lo:[0,1] neg_hi:[0,1]
	v_bitop3_b32 v30, v86, s1, v88 bitop3:0x6c
	v_pk_add_f32 v[28:29], v[28:29], s[50:51] op_sel_hi:[1,0] neg_lo:[0,1] neg_hi:[0,1]
	v_mul_f32_e32 v94, v33, v33
	v_or3_b32 v137, v85, v30, v87
	v_pk_add_f32 v[30:31], v[26:27], s[50:51] op_sel_hi:[1,0] neg_lo:[0,1] neg_hi:[0,1]
	v_mul_f32_e32 v26, v29, v29
	v_fmac_f32_e32 v94, v32, v32
	v_fmac_f32_e32 v26, v28, v28
	v_fmac_f32_e32 v94, v35, v35
	v_fmac_f32_e32 v26, v31, v31
	v_fmac_f32_e32 v94, v34, v34
	v_fmac_f32_e32 v26, v30, v30
	v_cndmask_b32_e64 v27, v26, v94, s[4:5]
	v_cndmask_b32_e64 v26, v94, v26, s[4:5]
	s_movk_i32 s1, 0xb0
	v_pk_add_f32 v[24:25], v[24:25], s[52:53] op_sel_hi:[1,0] neg_lo:[0,1] neg_hi:[0,1]
	v_add_f32_dpp v26, v27, v26 quad_perm:[1,0,3,2] row_mask:0xf bank_mask:0xf bound_ctrl:1
	v_cndmask_b32_e64 v27, v89, v26, s[6:7]
	v_cndmask_b32_e64 v26, v26, v89, s[6:7]
	v_pk_add_f32 v[20:21], v[20:21], s[54:55] op_sel_hi:[1,0] neg_lo:[0,1] neg_hi:[0,1]
	v_mul_f32_e32 v94, v25, v25
	v_add_f32_dpp v89, v27, v26 quad_perm:[2,3,0,1] row_mask:0xf bank_mask:0xf bound_ctrl:1
	v_bitop3_b32 v26, v86, s1, v88 bitop3:0x6c
	s_movk_i32 s1, 0xc0
	v_or3_b32 v136, v85, v26, v87
	v_pk_add_f32 v[26:27], v[22:23], s[52:53] op_sel_hi:[1,0] neg_lo:[0,1] neg_hi:[0,1]
	v_bitop3_b32 v22, v86, s1, v88 bitop3:0x6c
	v_or3_b32 v123, v85, v22, v87
	v_pk_add_f32 v[22:23], v[18:19], s[54:55] op_sel_hi:[1,0] neg_lo:[0,1] neg_hi:[0,1]
	v_mul_f32_e32 v18, v21, v21
	v_fmac_f32_e32 v94, v24, v24
	v_fmac_f32_e32 v18, v20, v20
	v_fmac_f32_e32 v94, v27, v27
	v_fmac_f32_e32 v18, v23, v23
	v_fmac_f32_e32 v94, v26, v26
	v_fmac_f32_e32 v18, v22, v22
	v_cndmask_b32_e64 v19, v18, v94, s[4:5]
	v_cndmask_b32_e64 v18, v94, v18, s[4:5]
	v_pk_add_f32 v[16:17], v[16:17], s[42:43] op_sel_hi:[1,0] neg_lo:[0,1] neg_hi:[0,1]
	s_nop 0
	v_add_f32_dpp v94, v19, v18 quad_perm:[1,0,3,2] row_mask:0xf bank_mask:0xf bound_ctrl:1
	v_pk_add_f32 v[18:19], v[14:15], s[42:43] op_sel_hi:[1,0] neg_lo:[0,1] neg_hi:[0,1]
	v_pk_add_f32 v[14:15], v[10:11], s[0:1] op_sel_hi:[1,0] neg_lo:[0,1] neg_hi:[0,1]
	v_pk_add_f32 v[10:11], v[12:13], s[0:1] op_sel_hi:[1,0] neg_lo:[0,1] neg_hi:[0,1]
	v_mul_f32_e32 v95, v17, v17
	v_mul_f32_e32 v12, v11, v11
	v_fmac_f32_e32 v95, v16, v16
	v_fmac_f32_e32 v12, v10, v10
	v_fmac_f32_e32 v95, v19, v19
	v_fmac_f32_e32 v12, v15, v15
	v_fmac_f32_e32 v95, v18, v18
	v_fmac_f32_e32 v12, v14, v14
	v_cndmask_b32_e64 v13, v12, v95, s[4:5]
	v_cndmask_b32_e64 v12, v95, v12, s[4:5]
	s_movk_i32 s0, 0xd0
	s_nop 0
	v_add_f32_dpp v12, v13, v12 quad_perm:[1,0,3,2] row_mask:0xf bank_mask:0xf bound_ctrl:1
	v_cndmask_b32_e64 v13, v94, v12, s[6:7]
	v_cndmask_b32_e64 v12, v12, v94, s[6:7]
	s_nop 1
	v_add_f32_dpp v12, v13, v12 quad_perm:[2,3,0,1] row_mask:0xf bank_mask:0xf bound_ctrl:1
	v_cndmask_b32_e64 v13, v89, v12, s[8:9]
	v_cndmask_b32_e64 v12, v12, v89, s[8:9]
	v_mov_b32_e32 v89, v13
	s_nop 1
	v_mov_b32_dpp v89, v89 row_shl:4 row_mask:0xf bank_mask:0x5
	s_nop 1
	v_mov_b32_dpp v89, v13 row_shr:4 row_mask:0xf bank_mask:0xa
	v_add_f32_e32 v12, v12, v89
	v_bitop3_b32 v89, v86, s0, v88 bitop3:0x6c
	v_or3_b32 v133, v85, v89, v87
	v_add_f32_dpp v12, v12, v12 row_ror:8 row_mask:0xf bank_mask:0xf bound_ctrl:1
	v_mov_b32_e32 v13, v12
	s_nop 1
	v_permlane16_swap_b32_e32 v12, v13
	v_add_f32_e32 v12, v12, v13
	v_mov_b32_e32 v13, v12
	s_nop 1
	v_permlane32_swap_b32_e32 v12, v13
	v_add_f32_e32 v12, v12, v13
	v_fmamk_f32 v12, v12, 0x3b800000, v116
	v_mul_f32_e32 v13, 0x4f800000, v12
	v_cmp_gt_f32_e32 vcc, s35, v12
	s_nop 1
	v_cndmask_b32_e32 v12, v12, v13, vcc
	v_sqrt_f32_e32 v13, v12
	s_nop 0
	v_add_u32_e32 v89, -1, v13
	v_fma_f32 v94, -v89, v13, v12
	v_cmp_ge_f32_e64 s[0:1], 0, v94
	v_add_u32_e32 v94, 1, v13
	s_nop 0
	v_cndmask_b32_e64 v89, v13, v89, s[0:1]
	v_fma_f32 v13, -v94, v13, v12
	v_cmp_lt_f32_e64 s[0:1], 0, v13
	s_nop 1
	v_cndmask_b32_e64 v13, v89, v94, s[0:1]
	v_mul_f32_e32 v89, 0x37800000, v13
	v_cndmask_b32_e32 v13, v13, v89, vcc
	v_cmp_class_f32_e32 vcc, v12, v117
	s_nop 1
	v_cndmask_b32_e32 v12, v13, v12, vcc
	v_div_scale_f32 v13, s[0:1], v12, v12, 1.0
	v_rcp_f32_e32 v89, v13
	s_movk_i32 s0, 0xe0
	v_bitop3_b32 v94, v86, s0, v88 bitop3:0x6c
	v_or3_b32 v119, v85, v94, v87
	v_fma_f32 v94, -v13, v89, 1.0
	v_fmac_f32_e32 v89, v94, v89
	v_div_scale_f32 v94, vcc, 1.0, v12, 1.0
	v_mul_f32_e32 v95, v94, v89
	v_fma_f32 v96, -v13, v95, v94
	v_fmac_f32_e32 v95, v96, v89
	v_fma_f32 v13, -v13, v95, v94
	v_div_fmas_f32 v13, v13, v89, v95
	v_div_fixup_f32 v12, v13, v12, 1.0
	s_nop 0
	v_readlane_b32 s0, v12, 0
	s_nop 1
	v_pk_mul_f32 v[38:39], s[0:1], v[38:39] op_sel_hi:[0,1]
	v_pk_fma_f32 v[38:39], v[38:39], v[238:239], v[242:243]
	v_pk_mul_f32 v[40:41], s[0:1], v[40:41] op_sel_hi:[0,1]
	v_fma_f32 v13, |v38|, s25, 1.0
	v_rcp_f32_e32 v96, v13
	v_fma_f32 v13, |v39|, s25, 1.0
	v_rcp_f32_e32 v97, v13
	v_pk_mul_f32 v[98:99], v[38:39], v[38:39]
	v_pk_fma_f32 v[40:41], v[40:41], v[240:241], v[244:245]
	v_mul_f32_e32 v13, 0xbf38aa3b, v98
	v_pk_fma_f32 v[100:101], v[96:97], s[22:23], v[90:91] op_sel_hi:[1,0,0]
	v_exp_f32_e32 v98, v13
	v_pk_fma_f32 v[100:101], v[96:97], v[100:101], s[24:25] op_sel_hi:[1,1,0]
	v_mul_f32_e32 v13, 0xbf38aa3b, v99
	v_pk_fma_f32 v[100:101], v[96:97], v[100:101], s[34:35] op_sel_hi:[1,1,0]
	v_and_b32_e32 v95, 0x7fffffff, v39
	v_pk_fma_f32 v[100:101], v[96:97], v[100:101], s[40:41] op_sel_hi:[1,1,0]
	v_and_b32_e32 v94, 0x7fffffff, v38
	v_exp_f32_e32 v99, v13
	v_pk_mul_f32 v[96:97], v[96:97], v[100:101]
	v_fma_f32 v13, |v40|, s25, 1.0
	v_pk_mul_f32 v[94:95], v[94:95], v[96:97]
	v_rcp_f32_e32 v96, v13
	v_fma_f32 v13, |v41|, s25, 1.0
	v_rcp_f32_e32 v97, v13
	v_max_f32_e32 v38, 0, v38
	v_max_f32_e32 v39, 0, v39
	v_pk_fma_f32 v[38:39], v[98:99], v[94:95], v[38:39] neg_lo:[1,0,0] neg_hi:[1,0,0]
	v_pk_mul_f32 v[98:99], v[40:41], v[40:41]
	v_pk_fma_f32 v[100:101], v[96:97], s[22:23], v[90:91] op_sel_hi:[1,0,0]
	v_mul_f32_e32 v13, 0xbf38aa3b, v98
	v_exp_f32_e32 v98, v13
	v_pk_fma_f32 v[100:101], v[96:97], v[100:101], s[24:25] op_sel_hi:[1,1,0]
	v_mul_f32_e32 v13, 0xbf38aa3b, v99
	v_pk_fma_f32 v[100:101], v[96:97], v[100:101], s[34:35] op_sel_hi:[1,1,0]
	v_exp_f32_e32 v99, v13
	v_pk_fma_f32 v[100:101], v[96:97], v[100:101], s[40:41] op_sel_hi:[1,1,0]
	v_and_b32_e32 v95, 0x7fffffff, v41
	v_and_b32_e32 v94, 0x7fffffff, v40
	v_pk_mul_f32 v[96:97], v[96:97], v[100:101]
	v_max_f32_e32 v40, 0, v40
	v_max_f32_e32 v41, 0, v41
	v_pk_mul_f32 v[94:95], v[94:95], v[96:97]
	v_cvt_pk_f16_f32 v38, v38, v39
	v_pk_fma_f32 v[40:41], v[98:99], v[94:95], v[40:41] neg_lo:[1,0,0] neg_hi:[1,0,0]
	v_readlane_b32 s0, v12, 1
	v_cvt_pk_f16_f32 v39, v40, v41
	ds_write_b64 v145, v[38:39] offset:36864
	v_pk_mul_f32 v[38:39], s[0:1], v[92:93] op_sel_hi:[0,1]
	v_pk_fma_f32 v[38:39], v[38:39], v[238:239], v[242:243]
	v_pk_mul_f32 v[36:37], s[0:1], v[36:37] op_sel_hi:[0,1]
	v_fma_f32 v13, |v38|, s25, 1.0
	v_rcp_f32_e32 v92, v13
	v_fma_f32 v13, |v39|, s25, 1.0
	v_rcp_f32_e32 v93, v13
	v_pk_mul_f32 v[94:95], v[38:39], v[38:39]
	v_pk_fma_f32 v[36:37], v[36:37], v[240:241], v[244:245]
	v_mul_f32_e32 v13, 0xbf38aa3b, v94
	v_pk_fma_f32 v[96:97], v[92:93], s[22:23], v[90:91] op_sel_hi:[1,0,0]
	v_exp_f32_e32 v94, v13
	v_pk_fma_f32 v[96:97], v[92:93], v[96:97], s[24:25] op_sel_hi:[1,1,0]
	v_mul_f32_e32 v13, 0xbf38aa3b, v95
	v_pk_fma_f32 v[96:97], v[92:93], v[96:97], s[34:35] op_sel_hi:[1,1,0]
	v_and_b32_e32 v41, 0x7fffffff, v39
	v_pk_fma_f32 v[96:97], v[92:93], v[96:97], s[40:41] op_sel_hi:[1,1,0]
	v_and_b32_e32 v40, 0x7fffffff, v38
	v_exp_f32_e32 v95, v13
	v_pk_mul_f32 v[92:93], v[92:93], v[96:97]
	v_fma_f32 v13, |v36|, s25, 1.0
	v_pk_mul_f32 v[40:41], v[40:41], v[92:93]
	v_rcp_f32_e32 v92, v13
	v_fma_f32 v13, |v37|, s25, 1.0
	v_rcp_f32_e32 v93, v13
	v_max_f32_e32 v38, 0, v38
	v_max_f32_e32 v39, 0, v39
	v_pk_fma_f32 v[38:39], v[94:95], v[40:41], v[38:39] neg_lo:[1,0,0] neg_hi:[1,0,0]
	v_pk_mul_f32 v[94:95], v[36:37], v[36:37]
	v_pk_fma_f32 v[96:97], v[92:93], s[22:23], v[90:91] op_sel_hi:[1,0,0]
	v_mul_f32_e32 v13, 0xbf38aa3b, v94
	v_exp_f32_e32 v94, v13
	v_pk_fma_f32 v[96:97], v[92:93], v[96:97], s[24:25] op_sel_hi:[1,1,0]
	v_mul_f32_e32 v13, 0xbf38aa3b, v95
	v_pk_fma_f32 v[96:97], v[92:93], v[96:97], s[34:35] op_sel_hi:[1,1,0]
	v_exp_f32_e32 v95, v13
	v_pk_fma_f32 v[96:97], v[92:93], v[96:97], s[40:41] op_sel_hi:[1,1,0]
	v_and_b32_e32 v41, 0x7fffffff, v37
	v_and_b32_e32 v40, 0x7fffffff, v36
	v_pk_mul_f32 v[92:93], v[92:93], v[96:97]
	v_readlane_b32 s0, v12, 2
	v_max_f32_e32 v36, 0, v36
	v_max_f32_e32 v37, 0, v37
	v_pk_mul_f32 v[40:41], v[40:41], v[92:93]
	v_pk_mul_f32 v[34:35], s[0:1], v[34:35] op_sel_hi:[0,1]
	v_pk_fma_f32 v[36:37], v[94:95], v[40:41], v[36:37] neg_lo:[1,0,0] neg_hi:[1,0,0]
	v_pk_fma_f32 v[34:35], v[34:35], v[238:239], v[242:243]
	v_cvt_pk_f16_f32 v38, v38, v39
	v_cvt_pk_f16_f32 v39, v36, v37
	v_fma_f32 v13, |v34|, s25, 1.0
	ds_write_b64 v139, v[38:39] offset:37376
	v_rcp_f32_e32 v38, v13
	v_fma_f32 v13, |v35|, s25, 1.0
	v_rcp_f32_e32 v39, v13
	v_pk_mul_f32 v[40:41], v[34:35], v[34:35]
	v_pk_mul_f32 v[32:33], s[0:1], v[32:33] op_sel_hi:[0,1]
	v_mul_f32_e32 v13, 0xbf38aa3b, v40
	v_pk_fma_f32 v[92:93], v[38:39], s[22:23], v[90:91] op_sel_hi:[1,0,0]
	v_exp_f32_e32 v40, v13
	v_pk_fma_f32 v[92:93], v[38:39], v[92:93], s[24:25] op_sel_hi:[1,1,0]
	v_mul_f32_e32 v13, 0xbf38aa3b, v41
	v_pk_fma_f32 v[92:93], v[38:39], v[92:93], s[34:35] op_sel_hi:[1,1,0]
	v_pk_fma_f32 v[32:33], v[32:33], v[240:241], v[244:245]
	v_pk_fma_f32 v[92:93], v[38:39], v[92:93], s[40:41] op_sel_hi:[1,1,0]
	v_and_b32_e32 v37, 0x7fffffff, v35
	v_and_b32_e32 v36, 0x7fffffff, v34
	v_exp_f32_e32 v41, v13
	v_pk_mul_f32 v[38:39], v[38:39], v[92:93]
	v_fma_f32 v13, |v32|, s25, 1.0
	v_pk_mul_f32 v[36:37], v[36:37], v[38:39]
	v_rcp_f32_e32 v38, v13
	v_fma_f32 v13, |v33|, s25, 1.0
	v_rcp_f32_e32 v39, v13
	v_max_f32_e32 v34, 0, v34
	v_max_f32_e32 v35, 0, v35
	v_pk_fma_f32 v[34:35], v[40:41], v[36:37], v[34:35] neg_lo:[1,0,0] neg_hi:[1,0,0]
	v_pk_mul_f32 v[40:41], v[32:33], v[32:33]
	v_pk_fma_f32 v[92:93], v[38:39], s[22:23], v[90:91] op_sel_hi:[1,0,0]
	v_mul_f32_e32 v13, 0xbf38aa3b, v40
	v_exp_f32_e32 v40, v13
	v_pk_fma_f32 v[92:93], v[38:39], v[92:93], s[24:25] op_sel_hi:[1,1,0]
	v_mul_f32_e32 v13, 0xbf38aa3b, v41
	v_pk_fma_f32 v[92:93], v[38:39], v[92:93], s[34:35] op_sel_hi:[1,1,0]
	v_exp_f32_e32 v41, v13
	v_pk_fma_f32 v[92:93], v[38:39], v[92:93], s[40:41] op_sel_hi:[1,1,0]
	v_and_b32_e32 v37, 0x7fffffff, v33
	v_and_b32_e32 v36, 0x7fffffff, v32
	v_pk_mul_f32 v[38:39], v[38:39], v[92:93]
	v_readlane_b32 s0, v12, 3
	v_max_f32_e32 v32, 0, v32
	v_max_f32_e32 v33, 0, v33
	v_pk_mul_f32 v[36:37], v[36:37], v[38:39]
	v_pk_mul_f32 v[30:31], s[0:1], v[30:31] op_sel_hi:[0,1]
	v_pk_fma_f32 v[32:33], v[40:41], v[36:37], v[32:33] neg_lo:[1,0,0] neg_hi:[1,0,0]
	v_pk_fma_f32 v[30:31], v[30:31], v[238:239], v[242:243]
	v_cvt_pk_f16_f32 v34, v34, v35
	v_cvt_pk_f16_f32 v35, v32, v33
	v_fma_f32 v13, |v30|, s25, 1.0
	ds_write_b64 v137, v[34:35] offset:37888
	v_rcp_f32_e32 v34, v13
	v_fma_f32 v13, |v31|, s25, 1.0
	v_rcp_f32_e32 v35, v13
	v_pk_mul_f32 v[36:37], v[30:31], v[30:31]
	v_pk_mul_f32 v[28:29], s[0:1], v[28:29] op_sel_hi:[0,1]
	v_mul_f32_e32 v13, 0xbf38aa3b, v36
	v_pk_fma_f32 v[38:39], v[34:35], s[22:23], v[90:91] op_sel_hi:[1,0,0]
	v_exp_f32_e32 v36, v13
	v_pk_fma_f32 v[38:39], v[34:35], v[38:39], s[24:25] op_sel_hi:[1,1,0]
	v_mul_f32_e32 v13, 0xbf38aa3b, v37
	v_pk_fma_f32 v[38:39], v[34:35], v[38:39], s[34:35] op_sel_hi:[1,1,0]
	v_pk_fma_f32 v[28:29], v[28:29], v[240:241], v[244:245]
	v_pk_fma_f32 v[38:39], v[34:35], v[38:39], s[40:41] op_sel_hi:[1,1,0]
	v_and_b32_e32 v33, 0x7fffffff, v31
	v_and_b32_e32 v32, 0x7fffffff, v30
	v_exp_f32_e32 v37, v13
	v_pk_mul_f32 v[34:35], v[34:35], v[38:39]
	v_fma_f32 v13, |v28|, s25, 1.0
	v_pk_mul_f32 v[32:33], v[32:33], v[34:35]
	v_rcp_f32_e32 v34, v13
	v_fma_f32 v13, |v29|, s25, 1.0
	v_rcp_f32_e32 v35, v13
	v_max_f32_e32 v30, 0, v30
	v_max_f32_e32 v31, 0, v31
	v_pk_fma_f32 v[30:31], v[36:37], v[32:33], v[30:31] neg_lo:[1,0,0] neg_hi:[1,0,0]
	v_pk_mul_f32 v[36:37], v[28:29], v[28:29]
	v_pk_fma_f32 v[38:39], v[34:35], s[22:23], v[90:91] op_sel_hi:[1,0,0]
	v_mul_f32_e32 v13, 0xbf38aa3b, v36
	v_exp_f32_e32 v36, v13
	v_pk_fma_f32 v[38:39], v[34:35], v[38:39], s[24:25] op_sel_hi:[1,1,0]
	v_mul_f32_e32 v13, 0xbf38aa3b, v37
	v_pk_fma_f32 v[38:39], v[34:35], v[38:39], s[34:35] op_sel_hi:[1,1,0]
	v_exp_f32_e32 v37, v13
	v_pk_fma_f32 v[38:39], v[34:35], v[38:39], s[40:41] op_sel_hi:[1,1,0]
	v_and_b32_e32 v33, 0x7fffffff, v29
	v_and_b32_e32 v32, 0x7fffffff, v28
	v_pk_mul_f32 v[34:35], v[34:35], v[38:39]
	v_readlane_b32 s0, v12, 4
	v_max_f32_e32 v28, 0, v28
	v_max_f32_e32 v29, 0, v29
	v_pk_mul_f32 v[32:33], v[32:33], v[34:35]
	v_pk_mul_f32 v[26:27], s[0:1], v[26:27] op_sel_hi:[0,1]
	v_pk_fma_f32 v[28:29], v[36:37], v[32:33], v[28:29] neg_lo:[1,0,0] neg_hi:[1,0,0]
	v_pk_fma_f32 v[26:27], v[26:27], v[238:239], v[242:243]
	v_cvt_pk_f16_f32 v30, v30, v31
	v_cvt_pk_f16_f32 v31, v28, v29
	v_fma_f32 v13, |v26|, s25, 1.0
	ds_write_b64 v136, v[30:31] offset:38400
	v_rcp_f32_e32 v30, v13
	v_fma_f32 v13, |v27|, s25, 1.0
	v_rcp_f32_e32 v31, v13
	v_pk_mul_f32 v[32:33], v[26:27], v[26:27]
	v_pk_mul_f32 v[24:25], s[0:1], v[24:25] op_sel_hi:[0,1]
	v_mul_f32_e32 v13, 0xbf38aa3b, v32
	v_pk_fma_f32 v[34:35], v[30:31], s[22:23], v[90:91] op_sel_hi:[1,0,0]
	v_exp_f32_e32 v32, v13
	v_pk_fma_f32 v[34:35], v[30:31], v[34:35], s[24:25] op_sel_hi:[1,1,0]
	v_mul_f32_e32 v13, 0xbf38aa3b, v33
	v_pk_fma_f32 v[34:35], v[30:31], v[34:35], s[34:35] op_sel_hi:[1,1,0]
	v_pk_fma_f32 v[24:25], v[24:25], v[240:241], v[244:245]
	v_pk_fma_f32 v[34:35], v[30:31], v[34:35], s[40:41] op_sel_hi:[1,1,0]
	v_and_b32_e32 v29, 0x7fffffff, v27
	v_and_b32_e32 v28, 0x7fffffff, v26
	v_exp_f32_e32 v33, v13
	v_pk_mul_f32 v[30:31], v[30:31], v[34:35]
	v_fma_f32 v13, |v24|, s25, 1.0
	v_pk_mul_f32 v[28:29], v[28:29], v[30:31]
	v_rcp_f32_e32 v30, v13
	v_fma_f32 v13, |v25|, s25, 1.0
	v_rcp_f32_e32 v31, v13
	v_max_f32_e32 v26, 0, v26
	v_max_f32_e32 v27, 0, v27
	v_pk_fma_f32 v[26:27], v[32:33], v[28:29], v[26:27] neg_lo:[1,0,0] neg_hi:[1,0,0]
	v_pk_mul_f32 v[32:33], v[24:25], v[24:25]
	v_pk_fma_f32 v[34:35], v[30:31], s[22:23], v[90:91] op_sel_hi:[1,0,0]
	v_mul_f32_e32 v13, 0xbf38aa3b, v32
	v_exp_f32_e32 v32, v13
	v_pk_fma_f32 v[34:35], v[30:31], v[34:35], s[24:25] op_sel_hi:[1,1,0]
	v_mul_f32_e32 v13, 0xbf38aa3b, v33
	v_pk_fma_f32 v[34:35], v[30:31], v[34:35], s[34:35] op_sel_hi:[1,1,0]
	v_exp_f32_e32 v33, v13
	v_pk_fma_f32 v[34:35], v[30:31], v[34:35], s[40:41] op_sel_hi:[1,1,0]
	v_and_b32_e32 v29, 0x7fffffff, v25
	v_and_b32_e32 v28, 0x7fffffff, v24
	v_pk_mul_f32 v[30:31], v[30:31], v[34:35]
	v_readlane_b32 s0, v12, 5
	v_max_f32_e32 v24, 0, v24
	v_max_f32_e32 v25, 0, v25
	v_pk_mul_f32 v[28:29], v[28:29], v[30:31]
	v_pk_mul_f32 v[22:23], s[0:1], v[22:23] op_sel_hi:[0,1]
	v_pk_fma_f32 v[24:25], v[32:33], v[28:29], v[24:25] neg_lo:[1,0,0] neg_hi:[1,0,0]
	v_pk_fma_f32 v[22:23], v[22:23], v[238:239], v[242:243]
	v_cvt_pk_f16_f32 v26, v26, v27
	v_cvt_pk_f16_f32 v27, v24, v25
	v_fma_f32 v13, |v22|, s25, 1.0
	ds_write_b64 v123, v[26:27] offset:38912
	v_rcp_f32_e32 v26, v13
	v_fma_f32 v13, |v23|, s25, 1.0
	v_rcp_f32_e32 v27, v13
	v_pk_mul_f32 v[28:29], v[22:23], v[22:23]
	v_pk_mul_f32 v[20:21], s[0:1], v[20:21] op_sel_hi:[0,1]
	v_mul_f32_e32 v13, 0xbf38aa3b, v28
	v_pk_fma_f32 v[30:31], v[26:27], s[22:23], v[90:91] op_sel_hi:[1,0,0]
	v_exp_f32_e32 v28, v13
	v_pk_fma_f32 v[30:31], v[26:27], v[30:31], s[24:25] op_sel_hi:[1,1,0]
	v_mul_f32_e32 v13, 0xbf38aa3b, v29
	v_pk_fma_f32 v[30:31], v[26:27], v[30:31], s[34:35] op_sel_hi:[1,1,0]
	v_pk_fma_f32 v[20:21], v[20:21], v[240:241], v[244:245]
	v_pk_fma_f32 v[30:31], v[26:27], v[30:31], s[40:41] op_sel_hi:[1,1,0]
	s_waitcnt vmcnt(7)
	v_add_f32_e32 v92, v170, v171
	v_add_f32_e32 v93, v172, v173
	v_and_b32_e32 v25, 0x7fffffff, v23
	v_and_b32_e32 v24, 0x7fffffff, v22
	v_exp_f32_e32 v29, v13
	v_pk_mul_f32 v[26:27], v[26:27], v[30:31]
	v_fma_f32 v13, |v20|, s25, 1.0
	v_add_f32_e32 v92, v92, v93
	s_waitcnt vmcnt(6)
	v_add_f32_e32 v93, v174, v175
	v_add_f32_e32 v94, v176, v177
	v_pk_mul_f32 v[24:25], v[24:25], v[26:27]
	v_rcp_f32_e32 v26, v13
	v_fma_f32 v13, |v21|, s25, 1.0
	v_add_f32_e32 v93, v93, v94
	s_waitcnt vmcnt(5)
	v_add_f32_e32 v94, v178, v179
	v_add_f32_e32 v95, v180, v181
	v_rcp_f32_e32 v27, v13
	v_add_f32_e32 v94, v94, v95
	s_waitcnt vmcnt(4)
	v_add_f32_e32 v95, v182, v183
	v_add_f32_e32 v96, v184, v185
	v_add_f32_e32 v95, v95, v96
	s_waitcnt vmcnt(3)
	v_add_f32_e32 v96, v186, v187
	v_add_f32_e32 v97, v188, v189
	v_max_f32_e32 v22, 0, v22
	v_max_f32_e32 v23, 0, v23
	v_add_f32_e32 v96, v96, v97
	s_waitcnt vmcnt(2)
	v_add_f32_e32 v97, v190, v191
	v_add_f32_e32 v98, v192, v193
	v_pk_fma_f32 v[22:23], v[28:29], v[24:25], v[22:23] neg_lo:[1,0,0] neg_hi:[1,0,0]
	v_pk_mul_f32 v[28:29], v[20:21], v[20:21]
	v_add_f32_e32 v97, v97, v98
	s_waitcnt vmcnt(1)
	v_add_f32_e32 v98, v194, v195
	v_add_f32_e32 v99, v196, v197
	v_mul_f32_e32 v13, 0xbf38aa3b, v28
	v_pk_fma_f32 v[30:31], v[26:27], s[22:23], v[90:91] op_sel_hi:[1,0,0]
	v_add_f32_e32 v98, v98, v99
	s_waitcnt vmcnt(0)
	v_add_f32_e32 v99, v198, v199
	v_add_f32_e32 v100, v200, v201
	v_exp_f32_e32 v28, v13
	v_pk_fma_f32 v[30:31], v[26:27], v[30:31], s[24:25] op_sel_hi:[1,1,0]
	v_mul_f32_e32 v13, 0xbf38aa3b, v29
	v_add_f32_e32 v99, v99, v100
	v_cndmask_b32_e64 v100, v93, v92, s[4:5]
	v_cndmask_b32_e64 v92, v92, v93, s[4:5]
	v_cndmask_b32_e64 v93, v95, v94, s[4:5]
	v_cndmask_b32_e64 v94, v94, v95, s[4:5]
	v_pk_fma_f32 v[30:31], v[26:27], v[30:31], s[34:35] op_sel_hi:[1,1,0]
	v_exp_f32_e32 v29, v13
	v_add_f32_dpp v93, v93, v94 quad_perm:[1,0,3,2] row_mask:0xf bank_mask:0xf bound_ctrl:1
	v_cndmask_b32_e64 v94, v97, v96, s[4:5]
	v_cndmask_b32_e64 v95, v96, v97, s[4:5]
	v_pk_fma_f32 v[30:31], v[26:27], v[30:31], s[40:41] op_sel_hi:[1,1,0]
	v_cndmask_b32_e64 v96, v98, v99, s[4:5]
	v_add_f32_dpp v94, v94, v95 quad_perm:[1,0,3,2] row_mask:0xf bank_mask:0xf bound_ctrl:1
	v_cndmask_b32_e64 v95, v99, v98, s[4:5]
	v_and_b32_e32 v25, 0x7fffffff, v21
	v_and_b32_e32 v24, 0x7fffffff, v20
	v_pk_mul_f32 v[26:27], v[26:27], v[30:31]
	v_readlane_b32 s0, v12, 6
	v_add_f32_dpp v92, v100, v92 quad_perm:[1,0,3,2] row_mask:0xf bank_mask:0xf bound_ctrl:1
	v_add_f32_dpp v95, v95, v96 quad_perm:[1,0,3,2] row_mask:0xf bank_mask:0xf bound_ctrl:1
	v_max_f32_e32 v20, 0, v20
	v_max_f32_e32 v21, 0, v21
	v_pk_mul_f32 v[24:25], v[24:25], v[26:27]
	v_pk_mul_f32 v[18:19], s[0:1], v[18:19] op_sel_hi:[0,1]
	v_cndmask_b32_e64 v96, v92, v93, s[6:7]
	v_cndmask_b32_e64 v92, v93, v92, s[6:7]
	v_cndmask_b32_e64 v93, v94, v95, s[6:7]
	v_cndmask_b32_e64 v94, v95, v94, s[6:7]
	v_pk_fma_f32 v[20:21], v[28:29], v[24:25], v[20:21] neg_lo:[1,0,0] neg_hi:[1,0,0]
	v_pk_fma_f32 v[18:19], v[18:19], v[238:239], v[242:243]
	v_add_f32_dpp v92, v96, v92 quad_perm:[2,3,0,1] row_mask:0xf bank_mask:0xf bound_ctrl:1
	v_add_f32_dpp v93, v93, v94 quad_perm:[2,3,0,1] row_mask:0xf bank_mask:0xf bound_ctrl:1
	v_cvt_pk_f16_f32 v22, v22, v23
	v_cvt_pk_f16_f32 v23, v20, v21
	v_fma_f32 v13, |v18|, s25, 1.0
	v_cndmask_b32_e64 v94, v92, v93, s[8:9]
	ds_write_b64 v133, v[22:23] offset:39424
	v_rcp_f32_e32 v22, v13
	v_fma_f32 v13, |v19|, s25, 1.0
	v_cndmask_b32_e64 v92, v93, v92, s[8:9]
	v_mov_b32_e32 v93, v94
	v_rcp_f32_e32 v23, v13
	v_pk_mul_f32 v[24:25], v[18:19], v[18:19]
	v_mov_b32_dpp v93, v93 row_shl:4 row_mask:0xf bank_mask:0x5
	v_mul_f32_e32 v13, 0xbf38aa3b, v24
	v_pk_fma_f32 v[26:27], v[22:23], s[22:23], v[90:91] op_sel_hi:[1,0,0]
	v_mov_b32_dpp v93, v94 row_shr:4 row_mask:0xf bank_mask:0xa
	v_add_f32_e32 v92, v92, v93
	v_pk_fma_f32 v[26:27], v[22:23], v[26:27], s[24:25] op_sel_hi:[1,1,0]
	v_pk_mul_f32 v[16:17], s[0:1], v[16:17] op_sel_hi:[0,1]
	v_add_f32_dpp v92, v92, v92 row_ror:8 row_mask:0xf bank_mask:0xf bound_ctrl:1
	v_mov_b32_e32 v93, v92
	s_nop 1
	v_permlane16_swap_b32_e32 v92, v93
	v_pk_fma_f32 v[26:27], v[22:23], v[26:27], s[34:35] op_sel_hi:[1,1,0]
	v_add_f32_e32 v92, v92, v93
	v_exp_f32_e32 v24, v13
	v_pk_fma_f32 v[26:27], v[22:23], v[26:27], s[40:41] op_sel_hi:[1,1,0]
	v_mul_f32_e32 v13, 0xbf38aa3b, v25
	v_pk_fma_f32 v[16:17], v[16:17], v[240:241], v[244:245]
	v_mov_b32_e32 v93, v92
	v_and_b32_e32 v21, 0x7fffffff, v19
	v_and_b32_e32 v20, 0x7fffffff, v18
	v_exp_f32_e32 v25, v13
	v_pk_mul_f32 v[22:23], v[22:23], v[26:27]
	v_fma_f32 v13, |v16|, s25, 1.0
	v_permlane32_swap_b32_e32 v92, v93
	v_pk_mul_f32 v[20:21], v[20:21], v[22:23]
	v_rcp_f32_e32 v22, v13
	v_fma_f32 v13, |v17|, s25, 1.0
	v_add_f32_e32 v92, v92, v93
	v_rcp_f32_e32 v23, v13
	v_mul_f32_e32 v92, 0x3b800000, v92
	v_max_f32_e32 v18, 0, v18
	v_max_f32_e32 v19, 0, v19
	v_readlane_b32 s42, v92, 0
	v_readlane_b32 s44, v92, 1
	v_readlane_b32 s46, v92, 2
	v_readlane_b32 s48, v92, 3
	v_pk_fma_f32 v[18:19], v[24:25], v[20:21], v[18:19] neg_lo:[1,0,0] neg_hi:[1,0,0]
	v_pk_mul_f32 v[24:25], v[16:17], v[16:17]
	v_pk_add_f32 v[160:161], v[172:173], s[42:43] op_sel_hi:[1, 0] neg_lo:[0, 1] neg_hi:[0, 1]
	v_pk_add_f32 v[110:111], v[176:177], s[44:45] op_sel_hi:[1, 0] neg_lo:[0, 1] neg_hi:[0, 1]
	v_pk_add_f32 v[104:105], v[180:181], s[46:47] op_sel_hi:[1, 0] neg_lo:[0, 1] neg_hi:[0, 1]
	v_pk_add_f32 v[100:101], v[184:185], s[48:49] op_sel_hi:[1, 0] neg_lo:[0, 1] neg_hi:[0, 1]
	v_mul_f32_e32 v13, 0xbf38aa3b, v24
	v_pk_add_f32 v[158:159], v[170:171], s[42:43] op_sel_hi:[1, 0] neg_lo:[0, 1] neg_hi:[0, 1]
	v_mul_f32_e32 v78, v161, v161
	v_pk_add_f32 v[162:163], v[174:175], s[44:45] op_sel_hi:[1, 0] neg_lo:[0, 1] neg_hi:[0, 1]
	v_mul_f32_e32 v74, v111, v111
	v_pk_add_f32 v[108:109], v[178:179], s[46:47] op_sel_hi:[1, 0] neg_lo:[0, 1] neg_hi:[0, 1]
	v_mul_f32_e32 v70, v105, v105
	v_pk_add_f32 v[102:103], v[182:183], s[48:49] op_sel_hi:[1, 0] neg_lo:[0, 1] neg_hi:[0, 1]
	v_mul_f32_e32 v66, v101, v101
	v_exp_f32_e32 v24, v13
	v_pk_fma_f32 v[26:27], v[22:23], s[22:23], v[90:91] op_sel_hi:[1,0,0]
	v_mul_f32_e32 v13, 0xbf38aa3b, v25
	v_readlane_b32 s0, v12, 7
	v_fmac_f32_e32 v78, v160, v160
	v_fmac_f32_e32 v74, v110, v110
	v_fmac_f32_e32 v70, v104, v104
	v_fmac_f32_e32 v66, v100, v100
	v_pk_fma_f32 v[26:27], v[22:23], v[26:27], s[24:25] op_sel_hi:[1,1,0]
	v_exp_f32_e32 v25, v13
	v_pk_mul_f32 v[12:13], s[0:1], v[14:15] op_sel_hi:[0,1]
	v_pk_mul_f32 v[10:11], s[0:1], v[10:11] op_sel_hi:[0,1]
	s_movk_i32 s0, 0x6000
	v_fmac_f32_e32 v78, v159, v159
	v_fmac_f32_e32 v74, v163, v163
	v_fmac_f32_e32 v70, v109, v109
	v_fmac_f32_e32 v66, v103, v103
	v_pk_fma_f32 v[26:27], v[22:23], v[26:27], s[34:35] op_sel_hi:[1,1,0]
	v_add_co_u32_e32 v154, vcc, s0, v82
	v_fmac_f32_e32 v78, v158, v158
	v_fmac_f32_e32 v74, v162, v162
	v_fmac_f32_e32 v70, v108, v108
	v_fmac_f32_e32 v66, v102, v102
	v_pk_fma_f32 v[26:27], v[22:23], v[26:27], s[40:41] op_sel_hi:[1,1,0]
	v_addc_co_u32_e32 v155, vcc, 0, v83, vcc
	s_movk_i32 s0, 0x7000
	v_cndmask_b32_e64 v75, v74, v78, s[4:5]
	v_cndmask_b32_e64 v74, v78, v74, s[4:5]
	v_cndmask_b32_e64 v67, v66, v70, s[4:5]
	v_cndmask_b32_e64 v66, v70, v66, s[4:5]
	v_and_b32_e32 v21, 0x7fffffff, v17
	v_and_b32_e32 v20, 0x7fffffff, v16
	v_pk_mul_f32 v[22:23], v[22:23], v[26:27]
	v_add_co_u32_e32 v156, vcc, s0, v82
	v_readlane_b32 s50, v92, 4
	v_readlane_b32 s52, v92, 5
	v_readlane_b32 s54, v92, 6
	v_readlane_b32 s0, v92, 7
	v_add_f32_dpp v74, v75, v74 quad_perm:[1,0,3,2] row_mask:0xf bank_mask:0xf bound_ctrl:1
	v_add_f32_dpp v66, v67, v66 quad_perm:[1,0,3,2] row_mask:0xf bank_mask:0xf bound_ctrl:1
	v_max_f32_e32 v16, 0, v16
	v_max_f32_e32 v17, 0, v17
	v_pk_mul_f32 v[20:21], v[20:21], v[22:23]
	v_cndmask_b32_e64 v67, v74, v66, s[6:7]
	v_cndmask_b32_e64 v66, v66, v74, s[6:7]
	v_pk_add_f32 v[96:97], v[188:189], s[50:51] op_sel_hi:[1, 0] neg_lo:[0, 1] neg_hi:[0, 1]
	v_pk_add_f32 v[92:93], v[192:193], s[52:53] op_sel_hi:[1, 0] neg_lo:[0, 1] neg_hi:[0, 1]
	v_pk_add_f32 v[78:79], v[196:197], s[54:55] op_sel_hi:[1, 0] neg_lo:[0, 1] neg_hi:[0, 1]
	v_pk_add_f32 v[74:75], v[200:201], s[0:1] op_sel_hi:[1, 0] neg_lo:[0, 1] neg_hi:[0, 1]
	v_pk_fma_f32 v[16:17], v[24:25], v[20:21], v[16:17] neg_lo:[1,0,0] neg_hi:[1,0,0]
	v_pk_fma_f32 v[12:13], v[12:13], v[238:239], v[242:243]
	v_pk_add_f32 v[98:99], v[186:187], s[50:51] op_sel_hi:[1, 0] neg_lo:[0, 1] neg_hi:[0, 1]
	v_mul_f32_e32 v62, v97, v97
	v_pk_add_f32 v[94:95], v[190:191], s[52:53] op_sel_hi:[1, 0] neg_lo:[0, 1] neg_hi:[0, 1]
	v_mul_f32_e32 v58, v93, v93
	v_pk_add_f32 v[80:81], v[194:195], s[54:55] op_sel_hi:[1, 0] neg_lo:[0, 1] neg_hi:[0, 1]
	v_mul_f32_e32 v54, v79, v79
	v_pk_add_f32 v[76:77], v[198:199], s[0:1] op_sel_hi:[1, 0] neg_lo:[0, 1] neg_hi:[0, 1]
	v_mul_f32_e32 v50, v75, v75
	v_cvt_pk_f16_f32 v18, v18, v19
	v_cvt_pk_f16_f32 v19, v16, v17
	v_fma_f32 v16, |v12|, s25, 1.0
	v_fma_f32 v17, |v13|, s25, 1.0
	v_fmac_f32_e32 v62, v96, v96
	v_fmac_f32_e32 v58, v92, v92
	v_fmac_f32_e32 v54, v78, v78
	v_fmac_f32_e32 v50, v74, v74
	v_rcp_f32_e32 v16, v16
	v_rcp_f32_e32 v17, v17
	v_fmac_f32_e32 v62, v99, v99
	v_fmac_f32_e32 v58, v95, v95
	v_fmac_f32_e32 v54, v81, v81
	v_fmac_f32_e32 v50, v77, v77
	v_fmac_f32_e32 v62, v98, v98
	v_fmac_f32_e32 v58, v94, v94
	v_fmac_f32_e32 v54, v80, v80
	v_fmac_f32_e32 v50, v76, v76
	v_cndmask_b32_e64 v59, v58, v62, s[4:5]
	v_cndmask_b32_e64 v58, v62, v58, s[4:5]
	v_cndmask_b32_e64 v51, v50, v54, s[4:5]
	v_cndmask_b32_e64 v50, v54, v50, s[4:5]
	v_add_f32_dpp v58, v59, v58 quad_perm:[1,0,3,2] row_mask:0xf bank_mask:0xf bound_ctrl:1
	ds_write_b64 v119, v[18:19] offset:39936
	v_add_f32_dpp v50, v51, v50 quad_perm:[1,0,3,2] row_mask:0xf bank_mask:0xf bound_ctrl:1
	v_pk_mul_f32 v[18:19], v[12:13], v[12:13]
	v_pk_fma_f32 v[20:21], v[16:17], s[22:23], v[90:91] op_sel_hi:[1,0,0]
	v_cndmask_b32_e64 v51, v58, v50, s[6:7]
	v_cndmask_b32_e64 v50, v50, v58, s[6:7]
	v_mul_f32_e32 v18, 0xbf38aa3b, v18
	v_pk_fma_f32 v[20:21], v[16:17], v[20:21], s[24:25] op_sel_hi:[1,1,0]
	v_mul_f32_e32 v19, 0xbf38aa3b, v19
	v_add_f32_dpp v66, v67, v66 quad_perm:[2,3,0,1] row_mask:0xf bank_mask:0xf bound_ctrl:1
	v_add_f32_dpp v50, v51, v50 quad_perm:[2,3,0,1] row_mask:0xf bank_mask:0xf bound_ctrl:1
	v_exp_f32_e32 v18, v18
	v_pk_fma_f32 v[20:21], v[16:17], v[20:21], s[34:35] op_sel_hi:[1,1,0]
	v_exp_f32_e32 v19, v19
	v_cndmask_b32_e64 v51, v66, v50, s[8:9]
	v_pk_fma_f32 v[20:21], v[16:17], v[20:21], s[40:41] op_sel_hi:[1,1,0]
	v_mov_b32_e32 v52, v51
	v_and_b32_e32 v15, 0x7fffffff, v13
	v_and_b32_e32 v14, 0x7fffffff, v12
	v_pk_mul_f32 v[16:17], v[16:17], v[20:21]
	v_mov_b32_dpp v52, v52 row_shl:4 row_mask:0xf bank_mask:0x5
	v_max_f32_e32 v12, 0, v12
	v_max_f32_e32 v13, 0, v13
	v_pk_mul_f32 v[14:15], v[14:15], v[16:17]
	v_cndmask_b32_e64 v50, v50, v66, s[8:9]
	v_mov_b32_dpp v52, v51 row_shr:4 row_mask:0xf bank_mask:0xa
	v_pk_fma_f32 v[12:13], v[18:19], v[14:15], v[12:13] neg_lo:[1,0,0] neg_hi:[1,0,0]
	v_pk_fma_f32 v[10:11], v[10:11], v[240:241], v[244:245]
	v_add_f32_e32 v50, v50, v52
	v_cvt_pk_f16_f32 v12, v12, v13
	v_fma_f32 v13, |v10|, s25, 1.0
	v_add_f32_dpp v50, v50, v50 row_ror:8 row_mask:0xf bank_mask:0xf bound_ctrl:1
	v_rcp_f32_e32 v16, v13
	v_fma_f32 v13, |v11|, s25, 1.0
	v_mov_b32_e32 v51, v50
	v_rcp_f32_e32 v17, v13
	s_nop 0
	v_permlane16_swap_b32_e32 v50, v51
	v_add_f32_e32 v50, v50, v51
	v_mov_b32_e32 v51, v50
	v_pk_mul_f32 v[18:19], v[10:11], v[10:11]
	s_nop 0
	v_permlane32_swap_b32_e32 v50, v51
	v_mul_f32_e32 v13, 0xbf38aa3b, v18
	v_pk_fma_f32 v[20:21], v[16:17], s[22:23], v[90:91] op_sel_hi:[1,0,0]
	v_add_f32_e32 v50, v50, v51
	v_exp_f32_e32 v18, v13
	v_pk_fma_f32 v[20:21], v[16:17], v[20:21], s[24:25] op_sel_hi:[1,1,0]
	v_mul_f32_e32 v13, 0xbf38aa3b, v19
	v_addc_co_u32_e32 v157, vcc, 0, v83, vcc
	v_fmamk_f32 v50, v50, 0x3b800000, v116
	v_pk_fma_f32 v[20:21], v[16:17], v[20:21], s[34:35] op_sel_hi:[1,1,0]
	v_exp_f32_e32 v19, v13
	v_mul_f32_e32 v51, 0x4f800000, v50
	v_cmp_gt_f32_e32 vcc, s35, v50
	v_pk_fma_f32 v[20:21], v[16:17], v[20:21], s[40:41] op_sel_hi:[1,1,0]
	v_and_b32_e32 v15, 0x7fffffff, v11
	v_cndmask_b32_e32 v50, v50, v51, vcc
	v_and_b32_e32 v14, 0x7fffffff, v10
	v_pk_mul_f32 v[16:17], v[16:17], v[20:21]
	v_sqrt_f32_e32 v51, v50
	v_max_f32_e32 v10, 0, v10
	v_max_f32_e32 v11, 0, v11
	v_pk_mul_f32 v[14:15], v[14:15], v[16:17]
	v_add_u32_e32 v52, -1, v51
	v_pk_fma_f32 v[10:11], v[18:19], v[14:15], v[10:11] neg_lo:[1,0,0] neg_hi:[1,0,0]
	v_fma_f32 v53, -v52, v51, v50
	v_cvt_pk_f16_f32 v13, v10, v11
	v_bitop3_b32 v10, v86, s41, v88 bitop3:0x6c
	v_or3_b32 v146, v85, v10, v87
	v_lshlrev_b32_e32 v10, 4, v141
	v_and_or_b32 v147, v10, s41, v84
	v_lshlrev_b32_e32 v10, 4, v142
	v_and_or_b32 v148, v10, s41, v84
	v_lshlrev_b32_e32 v10, 4, v143
	v_cmp_ge_f32_e64 s[0:1], 0, v53
	v_add_u32_e32 v53, 1, v51
	v_and_or_b32 v149, v10, s41, v84
	v_bitop3_b32 v10, v125, v0, 15 bitop3:0x78
	v_cndmask_b32_e64 v52, v51, v52, s[0:1]
	v_fma_f32 v51, -v53, v51, v50
	v_lshl_or_b32 v150, v10, 4, v84
	v_bitop3_b32 v10, v125, v107, 4 bitop3:0x36
	v_cmp_lt_f32_e64 s[0:1], 0, v51
	v_lshl_or_b32 v151, v10, 4, v84
	v_bitop3_b32 v10, v125, v107, 8 bitop3:0x36
	v_cndmask_b32_e64 v51, v52, v53, s[0:1]
	v_lshl_or_b32 v152, v10, 4, v84
	v_bitop3_b32 v10, v125, v107, 12 bitop3:0x36
	v_mul_f32_e32 v52, 0x37800000, v51
	ds_write_b64 v146, v[12:13] offset:40448
	v_lshl_or_b32 v153, v10, 4, v84
	v_cndmask_b32_e32 v51, v51, v52, vcc
	v_cmp_class_f32_e32 vcc, v50, v117
	ds_read_b128 v[38:41], v115 offset:32768
	ds_read_b128 v[34:37], v147 offset:32768
	ds_read_b128 v[30:33], v148 offset:32768
	ds_read_b128 v[26:29], v149 offset:32768
	ds_read_b128 v[22:25], v150 offset:33024
	ds_read_b128 v[18:21], v151 offset:33024
	ds_read_b128 v[14:17], v152 offset:33024
	ds_read_b128 v[10:13], v153 offset:33024
	s_movk_i32 s57, 0x7000
	s_nop 1
	v_add_co_u32_e64 v236, s[60:61], s57, v82
	s_nop 1
	v_addc_co_u32_e64 v237, s[60:61], 0, v83, s[60:61]
	s_nop 1
	global_load_dwordx4 v[206:209], v[236:237], off offset:-3072 nt
	global_load_dwordx4 v[210:213], v[236:237], off offset:-2048 nt
	global_load_dwordx4 v[214:217], v[236:237], off offset:-1024 nt
	global_load_dwordx4 v[202:205], v[236:237], off offset:-4096 nt
	global_load_dwordx4 v[218:221], v[236:237], off nt
	v_cndmask_b32_e32 v154, v51, v50, vcc
	v_div_scale_f32 v155, s[0:1], v154, v154, 1.0
	v_rcp_f32_e32 v164, v155
	global_load_dwordx4 v[222:225], v[236:237], off offset:1024 nt
	global_load_dwordx4 v[226:229], v[236:237], off offset:2048 nt
	global_load_dwordx4 v[230:233], v[236:237], off offset:3072 nt
	v_fma_f32 v156, -v155, v164, 1.0
	v_fmac_f32_e32 v164, v156, v164
	v_div_scale_f32 v156, vcc, 1.0, v154, 1.0
	v_mul_f32_e32 v157, v156, v164
	v_fma_f32 v165, -v155, v157, v156
	v_fmac_f32_e32 v157, v165, v164
	v_fma_f32 v155, -v155, v157, v156
	v_div_fmas_f32 v155, v155, v164, v157
	v_div_fixup_f32 v154, v155, v154, 1.0
	s_nop 0
	v_readlane_b32 s0, v154, 0
	s_nop 1
	v_pk_mul_f32 v[156:157], s[0:1], v[158:159] op_sel_hi:[0,1]
	v_pk_fma_f32 v[156:157], v[156:157], v[238:239], v[242:243]
	s_nop 0
	v_fma_f32 v155, |v156|, s25, 1.0
	v_rcp_f32_e32 v164, v155
	v_fma_f32 v155, |v157|, s25, 1.0
	v_rcp_f32_e32 v165, v155
	v_pk_mul_f32 v[166:167], v[156:157], v[156:157]
	v_and_b32_e32 v159, 0x7fffffff, v157
	v_mul_f32_e32 v155, 0xbf38aa3b, v166
	v_pk_fma_f32 v[168:169], v[164:165], s[22:23], v[90:91] op_sel_hi:[1,0,0]
	v_exp_f32_e32 v166, v155
	v_pk_fma_f32 v[168:169], v[164:165], v[168:169], s[24:25] op_sel_hi:[1,1,0]
	v_mul_f32_e32 v155, 0xbf38aa3b, v167
	v_pk_fma_f32 v[168:169], v[164:165], v[168:169], s[34:35] op_sel_hi:[1,1,0]
	v_exp_f32_e32 v167, v155
	v_pk_fma_f32 v[168:169], v[164:165], v[168:169], s[40:41] op_sel_hi:[1,1,0]
	v_and_b32_e32 v158, 0x7fffffff, v156
	v_pk_mul_f32 v[164:165], v[164:165], v[168:169]
	v_max_f32_e32 v156, 0, v156
	v_max_f32_e32 v157, 0, v157
	v_pk_mul_f32 v[158:159], v[158:159], v[164:165]
	s_nop 0
	v_pk_fma_f32 v[156:157], v[166:167], v[158:159], v[156:157] neg_lo:[1,0,0] neg_hi:[1,0,0]
	v_pk_mul_f32 v[158:159], s[0:1], v[160:161] op_sel_hi:[0,1]
	v_pk_fma_f32 v[158:159], v[158:159], v[240:241], v[244:245]
	v_cvt_pk_f16_f32 v156, v156, v157
	v_fma_f32 v155, |v158|, s25, 1.0
	v_rcp_f32_e32 v164, v155
	v_fma_f32 v155, |v159|, s25, 1.0
	v_rcp_f32_e32 v165, v155
	v_pk_mul_f32 v[166:167], v[158:159], v[158:159]
	v_and_b32_e32 v161, 0x7fffffff, v159
	v_mul_f32_e32 v155, 0xbf38aa3b, v166
	v_pk_fma_f32 v[168:169], v[164:165], s[22:23], v[90:91] op_sel_hi:[1,0,0]
	v_exp_f32_e32 v166, v155
	v_pk_fma_f32 v[168:169], v[164:165], v[168:169], s[24:25] op_sel_hi:[1,1,0]
	v_mul_f32_e32 v155, 0xbf38aa3b, v167
	v_pk_fma_f32 v[168:169], v[164:165], v[168:169], s[34:35] op_sel_hi:[1,1,0]
	v_exp_f32_e32 v167, v155
	v_pk_fma_f32 v[168:169], v[164:165], v[168:169], s[40:41] op_sel_hi:[1,1,0]
	v_and_b32_e32 v160, 0x7fffffff, v158
	v_pk_mul_f32 v[164:165], v[164:165], v[168:169]
	v_max_f32_e32 v158, 0, v158
	v_max_f32_e32 v159, 0, v159
	v_pk_mul_f32 v[160:161], v[160:161], v[164:165]
	v_readlane_b32 s0, v154, 1
	v_pk_fma_f32 v[158:159], v[166:167], v[160:161], v[158:159] neg_lo:[1,0,0] neg_hi:[1,0,0]
	s_nop 0
	v_cvt_pk_f16_f32 v157, v158, v159
	ds_write_b64 v140, v[156:157] offset:32768
	v_pk_mul_f32 v[156:157], s[0:1], v[162:163] op_sel_hi:[0,1]
	v_pk_fma_f32 v[156:157], v[156:157], v[238:239], v[242:243]
	v_pk_mul_f32 v[110:111], s[0:1], v[110:111] op_sel_hi:[0,1]
	v_fma_f32 v140, |v156|, s25, 1.0
	v_rcp_f32_e32 v160, v140
	v_fma_f32 v140, |v157|, s25, 1.0
	v_rcp_f32_e32 v161, v140
	v_pk_mul_f32 v[162:163], v[156:157], v[156:157]
	v_pk_fma_f32 v[110:111], v[110:111], v[240:241], v[244:245]
	v_mul_f32_e32 v140, 0xbf38aa3b, v162
	v_pk_fma_f32 v[164:165], v[160:161], s[22:23], v[90:91] op_sel_hi:[1,0,0]
	v_exp_f32_e32 v162, v140
	v_pk_fma_f32 v[164:165], v[160:161], v[164:165], s[24:25] op_sel_hi:[1,1,0]
	v_mul_f32_e32 v140, 0xbf38aa3b, v163
	v_pk_fma_f32 v[164:165], v[160:161], v[164:165], s[34:35] op_sel_hi:[1,1,0]
	v_and_b32_e32 v159, 0x7fffffff, v157
	v_pk_fma_f32 v[164:165], v[160:161], v[164:165], s[40:41] op_sel_hi:[1,1,0]
	v_and_b32_e32 v158, 0x7fffffff, v156
	v_exp_f32_e32 v163, v140
	v_pk_mul_f32 v[160:161], v[160:161], v[164:165]
	v_fma_f32 v140, |v110|, s25, 1.0
	v_pk_mul_f32 v[158:159], v[158:159], v[160:161]
	v_rcp_f32_e32 v160, v140
	v_fma_f32 v140, |v111|, s25, 1.0
	v_rcp_f32_e32 v161, v140
	v_max_f32_e32 v156, 0, v156
	v_max_f32_e32 v157, 0, v157
	v_pk_fma_f32 v[156:157], v[162:163], v[158:159], v[156:157] neg_lo:[1,0,0] neg_hi:[1,0,0]
	v_pk_mul_f32 v[162:163], v[110:111], v[110:111]
	v_pk_fma_f32 v[164:165], v[160:161], s[22:23], v[90:91] op_sel_hi:[1,0,0]
	v_mul_f32_e32 v140, 0xbf38aa3b, v162
	v_exp_f32_e32 v162, v140
	v_pk_fma_f32 v[164:165], v[160:161], v[164:165], s[24:25] op_sel_hi:[1,1,0]
	v_mul_f32_e32 v140, 0xbf38aa3b, v163
	v_pk_fma_f32 v[164:165], v[160:161], v[164:165], s[34:35] op_sel_hi:[1,1,0]
	v_exp_f32_e32 v163, v140
	v_pk_fma_f32 v[164:165], v[160:161], v[164:165], s[40:41] op_sel_hi:[1,1,0]
	v_and_b32_e32 v159, 0x7fffffff, v111
	v_and_b32_e32 v158, 0x7fffffff, v110
	v_pk_mul_f32 v[160:161], v[160:161], v[164:165]
	v_max_f32_e32 v110, 0, v110
	v_max_f32_e32 v111, 0, v111
	v_pk_mul_f32 v[158:159], v[158:159], v[160:161]
	v_readlane_b32 s0, v154, 2
	v_pk_fma_f32 v[110:111], v[162:163], v[158:159], v[110:111] neg_lo:[1,0,0] neg_hi:[1,0,0]
	v_cvt_pk_f16_f32 v156, v156, v157
	v_pk_mul_f32 v[108:109], s[0:1], v[108:109] op_sel_hi:[0,1]
	v_cvt_pk_f16_f32 v157, v110, v111
	v_pk_fma_f32 v[108:109], v[108:109], v[238:239], v[242:243]
	ds_write_b64 v138, v[156:157] offset:33280
	v_fma_f32 v138, |v108|, s25, 1.0
	v_rcp_f32_e32 v156, v138
	v_fma_f32 v138, |v109|, s25, 1.0
	v_rcp_f32_e32 v157, v138
	v_pk_mul_f32 v[158:159], v[108:109], v[108:109]
	v_and_b32_e32 v111, 0x7fffffff, v109
	v_mul_f32_e32 v138, 0xbf38aa3b, v158
	v_pk_fma_f32 v[160:161], v[156:157], s[22:23], v[90:91] op_sel_hi:[1,0,0]
	v_exp_f32_e32 v158, v138
	v_pk_fma_f32 v[160:161], v[156:157], v[160:161], s[24:25] op_sel_hi:[1,1,0]
	v_mul_f32_e32 v138, 0xbf38aa3b, v159
	v_pk_fma_f32 v[160:161], v[156:157], v[160:161], s[34:35] op_sel_hi:[1,1,0]
	v_exp_f32_e32 v159, v138
	v_pk_fma_f32 v[160:161], v[156:157], v[160:161], s[40:41] op_sel_hi:[1,1,0]
	v_and_b32_e32 v110, 0x7fffffff, v108
	v_pk_mul_f32 v[156:157], v[156:157], v[160:161]
	v_max_f32_e32 v108, 0, v108
	v_max_f32_e32 v109, 0, v109
	v_pk_mul_f32 v[110:111], v[110:111], v[156:157]
	v_pk_mul_f32 v[104:105], s[0:1], v[104:105] op_sel_hi:[0,1]
	v_pk_fma_f32 v[108:109], v[158:159], v[110:111], v[108:109] neg_lo:[1,0,0] neg_hi:[1,0,0]
	v_pk_fma_f32 v[104:105], v[104:105], v[240:241], v[244:245]
	v_cvt_pk_f16_f32 v108, v108, v109
	v_fma_f32 v109, |v104|, s25, 1.0
	v_rcp_f32_e32 v156, v109
	v_fma_f32 v109, |v105|, s25, 1.0
	v_rcp_f32_e32 v157, v109
	v_pk_mul_f32 v[158:159], v[104:105], v[104:105]
	v_and_b32_e32 v111, 0x7fffffff, v105
	v_mul_f32_e32 v109, 0xbf38aa3b, v158
	v_pk_fma_f32 v[160:161], v[156:157], s[22:23], v[90:91] op_sel_hi:[1,0,0]
	v_exp_f32_e32 v158, v109
	v_pk_fma_f32 v[160:161], v[156:157], v[160:161], s[24:25] op_sel_hi:[1,1,0]
	v_mul_f32_e32 v109, 0xbf38aa3b, v159
	v_pk_fma_f32 v[160:161], v[156:157], v[160:161], s[34:35] op_sel_hi:[1,1,0]
	v_exp_f32_e32 v159, v109
	v_pk_fma_f32 v[160:161], v[156:157], v[160:161], s[40:41] op_sel_hi:[1,1,0]
	v_and_b32_e32 v110, 0x7fffffff, v104
	v_pk_mul_f32 v[156:157], v[156:157], v[160:161]
	v_max_f32_e32 v104, 0, v104
	v_max_f32_e32 v105, 0, v105
	v_pk_mul_f32 v[110:111], v[110:111], v[156:157]
	v_readlane_b32 s0, v154, 3
	v_pk_fma_f32 v[104:105], v[158:159], v[110:111], v[104:105] neg_lo:[1,0,0] neg_hi:[1,0,0]
	s_nop 0
	v_pk_mul_f32 v[102:103], s[0:1], v[102:103] op_sel_hi:[0,1]
	v_cvt_pk_f16_f32 v109, v104, v105
	v_pk_fma_f32 v[102:103], v[102:103], v[238:239], v[242:243]
	ds_write_b64 v135, v[108:109] offset:33792
	v_fma_f32 v108, |v102|, s25, 1.0
	v_fma_f32 v109, |v103|, s25, 1.0
	v_rcp_f32_e32 v108, v108
	v_rcp_f32_e32 v109, v109
	v_pk_mul_f32 v[110:111], v[102:103], v[102:103]
	v_and_b32_e32 v105, 0x7fffffff, v103
	v_mul_f32_e32 v110, 0xbf38aa3b, v110
	v_pk_fma_f32 v[156:157], v[108:109], s[22:23], v[90:91] op_sel_hi:[1,0,0]
	v_mul_f32_e32 v111, 0xbf38aa3b, v111
	v_pk_fma_f32 v[156:157], v[108:109], v[156:157], s[24:25] op_sel_hi:[1,1,0]
	v_exp_f32_e32 v110, v110
	v_pk_fma_f32 v[156:157], v[108:109], v[156:157], s[34:35] op_sel_hi:[1,1,0]
	v_exp_f32_e32 v111, v111
	v_pk_fma_f32 v[156:157], v[108:109], v[156:157], s[40:41] op_sel_hi:[1,1,0]
	v_and_b32_e32 v104, 0x7fffffff, v102
	v_pk_mul_f32 v[108:109], v[108:109], v[156:157]
	v_max_f32_e32 v102, 0, v102
	v_max_f32_e32 v103, 0, v103
	v_pk_mul_f32 v[104:105], v[104:105], v[108:109]
	v_pk_mul_f32 v[100:101], s[0:1], v[100:101] op_sel_hi:[0,1]
	v_pk_fma_f32 v[102:103], v[110:111], v[104:105], v[102:103] neg_lo:[1,0,0] neg_hi:[1,0,0]
	v_pk_fma_f32 v[100:101], v[100:101], v[240:241], v[244:245]
	v_cvt_pk_f16_f32 v102, v102, v103
	v_fma_f32 v103, |v100|, s25, 1.0
	v_rcp_f32_e32 v108, v103
	v_fma_f32 v103, |v101|, s25, 1.0
	v_rcp_f32_e32 v109, v103
	v_pk_mul_f32 v[110:111], v[100:101], v[100:101]
	v_and_b32_e32 v105, 0x7fffffff, v101
	v_mul_f32_e32 v103, 0xbf38aa3b, v110
	v_pk_fma_f32 v[156:157], v[108:109], s[22:23], v[90:91] op_sel_hi:[1,0,0]
	v_exp_f32_e32 v110, v103
	v_pk_fma_f32 v[156:157], v[108:109], v[156:157], s[24:25] op_sel_hi:[1,1,0]
	v_mul_f32_e32 v103, 0xbf38aa3b, v111
	v_pk_fma_f32 v[156:157], v[108:109], v[156:157], s[34:35] op_sel_hi:[1,1,0]
	v_exp_f32_e32 v111, v103
	v_pk_fma_f32 v[156:157], v[108:109], v[156:157], s[40:41] op_sel_hi:[1,1,0]
	v_and_b32_e32 v104, 0x7fffffff, v100
	v_pk_mul_f32 v[108:109], v[108:109], v[156:157]
	v_max_f32_e32 v100, 0, v100
	v_max_f32_e32 v101, 0, v101
	v_pk_mul_f32 v[104:105], v[104:105], v[108:109]
	v_readlane_b32 s0, v154, 4
	v_pk_fma_f32 v[100:101], v[110:111], v[104:105], v[100:101] neg_lo:[1,0,0] neg_hi:[1,0,0]
	s_nop 0
	v_pk_mul_f32 v[98:99], s[0:1], v[98:99] op_sel_hi:[0,1]
	v_cvt_pk_f16_f32 v103, v100, v101
	v_pk_fma_f32 v[98:99], v[98:99], v[238:239], v[242:243]
	ds_write_b64 v134, v[102:103] offset:34304
	v_fma_f32 v102, |v98|, s25, 1.0
	v_fma_f32 v103, |v99|, s25, 1.0
	v_rcp_f32_e32 v102, v102
	v_rcp_f32_e32 v103, v103
	v_pk_mul_f32 v[104:105], v[98:99], v[98:99]
	v_and_b32_e32 v101, 0x7fffffff, v99
	v_mul_f32_e32 v104, 0xbf38aa3b, v104
	v_pk_fma_f32 v[108:109], v[102:103], s[22:23], v[90:91] op_sel_hi:[1,0,0]
	v_mul_f32_e32 v105, 0xbf38aa3b, v105
	v_pk_fma_f32 v[108:109], v[102:103], v[108:109], s[24:25] op_sel_hi:[1,1,0]
	v_exp_f32_e32 v104, v104
	v_pk_fma_f32 v[108:109], v[102:103], v[108:109], s[34:35] op_sel_hi:[1,1,0]
	v_exp_f32_e32 v105, v105
	v_pk_fma_f32 v[108:109], v[102:103], v[108:109], s[40:41] op_sel_hi:[1,1,0]
	v_and_b32_e32 v100, 0x7fffffff, v98
	v_pk_mul_f32 v[102:103], v[102:103], v[108:109]
	v_max_f32_e32 v98, 0, v98
	v_max_f32_e32 v99, 0, v99
	v_pk_mul_f32 v[100:101], v[100:101], v[102:103]
	v_pk_mul_f32 v[96:97], s[0:1], v[96:97] op_sel_hi:[0,1]
	v_pk_fma_f32 v[98:99], v[104:105], v[100:101], v[98:99] neg_lo:[1,0,0] neg_hi:[1,0,0]
	v_pk_fma_f32 v[96:97], v[96:97], v[240:241], v[244:245]
	v_cvt_pk_f16_f32 v98, v98, v99
	v_fma_f32 v99, |v96|, s25, 1.0
	v_rcp_f32_e32 v102, v99
	v_fma_f32 v99, |v97|, s25, 1.0
	v_rcp_f32_e32 v103, v99
	v_pk_mul_f32 v[104:105], v[96:97], v[96:97]
	v_and_b32_e32 v101, 0x7fffffff, v97
	v_mul_f32_e32 v99, 0xbf38aa3b, v104
	v_pk_fma_f32 v[108:109], v[102:103], s[22:23], v[90:91] op_sel_hi:[1,0,0]
	v_exp_f32_e32 v104, v99
	v_pk_fma_f32 v[108:109], v[102:103], v[108:109], s[24:25] op_sel_hi:[1,1,0]
	v_mul_f32_e32 v99, 0xbf38aa3b, v105
	v_pk_fma_f32 v[108:109], v[102:103], v[108:109], s[34:35] op_sel_hi:[1,1,0]
	v_exp_f32_e32 v105, v99
	v_pk_fma_f32 v[108:109], v[102:103], v[108:109], s[40:41] op_sel_hi:[1,1,0]
	v_and_b32_e32 v100, 0x7fffffff, v96
	v_pk_mul_f32 v[102:103], v[102:103], v[108:109]
	v_max_f32_e32 v96, 0, v96
	v_max_f32_e32 v97, 0, v97
	v_pk_mul_f32 v[100:101], v[100:101], v[102:103]
	v_readlane_b32 s0, v154, 5
	v_pk_fma_f32 v[96:97], v[104:105], v[100:101], v[96:97] neg_lo:[1,0,0] neg_hi:[1,0,0]
	v_mov_b32_e32 v104, 0
	v_pk_mul_f32 v[94:95], s[0:1], v[94:95] op_sel_hi:[0,1]
	v_cvt_pk_f16_f32 v99, v96, v97
	v_pk_fma_f32 v[94:95], v[94:95], v[238:239], v[242:243]
	ds_write_b64 v120, v[98:99] offset:34816
	v_fma_f32 v98, |v94|, s25, 1.0
	v_fma_f32 v99, |v95|, s25, 1.0
	v_rcp_f32_e32 v98, v98
	v_rcp_f32_e32 v99, v99
	v_pk_mul_f32 v[100:101], v[94:95], v[94:95]
	v_and_b32_e32 v97, 0x7fffffff, v95
	v_mul_f32_e32 v100, 0xbf38aa3b, v100
	v_pk_fma_f32 v[102:103], v[98:99], s[22:23], v[90:91] op_sel_hi:[1,0,0]
	v_mul_f32_e32 v101, 0xbf38aa3b, v101
	v_pk_fma_f32 v[102:103], v[98:99], v[102:103], s[24:25] op_sel_hi:[1,1,0]
	v_exp_f32_e32 v100, v100
	v_pk_fma_f32 v[102:103], v[98:99], v[102:103], s[34:35] op_sel_hi:[1,1,0]
	v_exp_f32_e32 v101, v101
	v_pk_fma_f32 v[102:103], v[98:99], v[102:103], s[40:41] op_sel_hi:[1,1,0]
	v_and_b32_e32 v96, 0x7fffffff, v94
	v_pk_mul_f32 v[98:99], v[98:99], v[102:103]
	v_max_f32_e32 v94, 0, v94
	v_max_f32_e32 v95, 0, v95
	v_pk_mul_f32 v[96:97], v[96:97], v[98:99]
	v_pk_mul_f32 v[92:93], s[0:1], v[92:93] op_sel_hi:[0,1]
	v_pk_fma_f32 v[94:95], v[100:101], v[96:97], v[94:95] neg_lo:[1,0,0] neg_hi:[1,0,0]
	v_pk_fma_f32 v[92:93], v[92:93], v[240:241], v[244:245]
	v_cvt_pk_f16_f32 v94, v94, v95
	v_fma_f32 v95, |v92|, s25, 1.0
	v_rcp_f32_e32 v98, v95
	v_fma_f32 v95, |v93|, s25, 1.0
	v_rcp_f32_e32 v99, v95
	v_pk_mul_f32 v[100:101], v[92:93], v[92:93]
	v_and_b32_e32 v97, 0x7fffffff, v93
	v_mul_f32_e32 v95, 0xbf38aa3b, v100
	v_pk_fma_f32 v[102:103], v[98:99], s[22:23], v[90:91] op_sel_hi:[1,0,0]
	v_exp_f32_e32 v100, v95
	v_pk_fma_f32 v[102:103], v[98:99], v[102:103], s[24:25] op_sel_hi:[1,1,0]
	v_mul_f32_e32 v95, 0xbf38aa3b, v101
	v_pk_fma_f32 v[102:103], v[98:99], v[102:103], s[34:35] op_sel_hi:[1,1,0]
	v_exp_f32_e32 v101, v95
	v_pk_fma_f32 v[102:103], v[98:99], v[102:103], s[40:41] op_sel_hi:[1,1,0]
	v_and_b32_e32 v96, 0x7fffffff, v92
	v_pk_mul_f32 v[98:99], v[98:99], v[102:103]
	v_max_f32_e32 v92, 0, v92
	v_max_f32_e32 v93, 0, v93
	v_pk_mul_f32 v[96:97], v[96:97], v[98:99]
	v_readlane_b32 s0, v154, 6
	v_pk_fma_f32 v[92:93], v[100:101], v[96:97], v[92:93] neg_lo:[1,0,0] neg_hi:[1,0,0]
	s_waitcnt vmcnt(1)
	v_add_f32_e32 v100, v228, v229
	v_pk_mul_f32 v[80:81], s[0:1], v[80:81] op_sel_hi:[0,1]
	v_cvt_pk_f16_f32 v95, v92, v93
	v_pk_fma_f32 v[80:81], v[80:81], v[238:239], v[242:243]
	ds_write_b64 v121, v[94:95] offset:35328
	v_fma_f32 v94, |v80|, s25, 1.0
	v_fma_f32 v95, |v81|, s25, 1.0
	v_rcp_f32_e32 v94, v94
	v_rcp_f32_e32 v95, v95
	v_pk_mul_f32 v[96:97], v[80:81], v[80:81]
	v_and_b32_e32 v93, 0x7fffffff, v81
	v_mul_f32_e32 v96, 0xbf38aa3b, v96
	v_pk_fma_f32 v[98:99], v[94:95], s[22:23], v[90:91] op_sel_hi:[1,0,0]
	v_mul_f32_e32 v97, 0xbf38aa3b, v97
	v_pk_fma_f32 v[98:99], v[94:95], v[98:99], s[24:25] op_sel_hi:[1,1,0]
	v_exp_f32_e32 v96, v96
	v_pk_fma_f32 v[98:99], v[94:95], v[98:99], s[34:35] op_sel_hi:[1,1,0]
	v_exp_f32_e32 v97, v97
	v_pk_fma_f32 v[98:99], v[94:95], v[98:99], s[40:41] op_sel_hi:[1,1,0]
	v_and_b32_e32 v92, 0x7fffffff, v80
	v_pk_mul_f32 v[94:95], v[94:95], v[98:99]
	v_max_f32_e32 v80, 0, v80
	v_max_f32_e32 v81, 0, v81
	v_pk_mul_f32 v[92:93], v[92:93], v[94:95]
	v_pk_mul_f32 v[78:79], s[0:1], v[78:79] op_sel_hi:[0,1]
	v_pk_fma_f32 v[80:81], v[96:97], v[92:93], v[80:81] neg_lo:[1,0,0] neg_hi:[1,0,0]
	v_pk_fma_f32 v[78:79], v[78:79], v[240:241], v[244:245]
	v_cvt_pk_f16_f32 v80, v80, v81
	v_fma_f32 v81, |v78|, s25, 1.0
	v_rcp_f32_e32 v94, v81
	v_fma_f32 v81, |v79|, s25, 1.0
	v_rcp_f32_e32 v95, v81
	v_pk_mul_f32 v[96:97], v[78:79], v[78:79]
	v_and_b32_e32 v93, 0x7fffffff, v79
	v_mul_f32_e32 v81, 0xbf38aa3b, v96
	v_pk_fma_f32 v[98:99], v[94:95], s[22:23], v[90:91] op_sel_hi:[1,0,0]
	v_exp_f32_e32 v96, v81
	v_pk_fma_f32 v[98:99], v[94:95], v[98:99], s[24:25] op_sel_hi:[1,1,0]
	v_mul_f32_e32 v81, 0xbf38aa3b, v97
	v_pk_fma_f32 v[98:99], v[94:95], v[98:99], s[34:35] op_sel_hi:[1,1,0]
	v_exp_f32_e32 v97, v81
	v_pk_fma_f32 v[98:99], v[94:95], v[98:99], s[40:41] op_sel_hi:[1,1,0]
	v_and_b32_e32 v92, 0x7fffffff, v78
	v_pk_mul_f32 v[94:95], v[94:95], v[98:99]
	v_max_f32_e32 v78, 0, v78
	v_max_f32_e32 v79, 0, v79
	v_pk_mul_f32 v[92:93], v[92:93], v[94:95]
	v_readlane_b32 s0, v154, 7
	v_pk_fma_f32 v[78:79], v[96:97], v[92:93], v[78:79] neg_lo:[1,0,0] neg_hi:[1,0,0]
	v_add_f32_e32 v97, v224, v225
	v_pk_mul_f32 v[76:77], s[0:1], v[76:77] op_sel_hi:[0,1]
	v_cvt_pk_f16_f32 v81, v78, v79
	v_pk_fma_f32 v[76:77], v[76:77], v[238:239], v[242:243]
	ds_write_b64 v118, v[80:81] offset:35840
	v_fma_f32 v80, |v76|, s25, 1.0
	v_fma_f32 v81, |v77|, s25, 1.0
	v_rcp_f32_e32 v80, v80
	v_rcp_f32_e32 v81, v81
	v_pk_mul_f32 v[92:93], v[76:77], v[76:77]
	v_and_b32_e32 v79, 0x7fffffff, v77
	v_mul_f32_e32 v92, 0xbf38aa3b, v92
	v_pk_fma_f32 v[94:95], v[80:81], s[22:23], v[90:91] op_sel_hi:[1,0,0]
	v_mul_f32_e32 v93, 0xbf38aa3b, v93
	v_pk_fma_f32 v[94:95], v[80:81], v[94:95], s[24:25] op_sel_hi:[1,1,0]
	v_exp_f32_e32 v92, v92
	v_pk_fma_f32 v[94:95], v[80:81], v[94:95], s[34:35] op_sel_hi:[1,1,0]
	v_exp_f32_e32 v93, v93
	v_pk_fma_f32 v[94:95], v[80:81], v[94:95], s[40:41] op_sel_hi:[1,1,0]
	v_and_b32_e32 v78, 0x7fffffff, v76
	v_pk_mul_f32 v[80:81], v[80:81], v[94:95]
	v_max_f32_e32 v76, 0, v76
	v_max_f32_e32 v77, 0, v77
	v_pk_mul_f32 v[78:79], v[78:79], v[80:81]
	v_pk_mul_f32 v[74:75], s[0:1], v[74:75] op_sel_hi:[0,1]
	v_pk_fma_f32 v[76:77], v[92:93], v[78:79], v[76:77] neg_lo:[1,0,0] neg_hi:[1,0,0]
	v_pk_fma_f32 v[92:93], v[74:75], v[240:241], v[244:245]
	v_cvt_pk_f16_f32 v80, v76, v77
	v_fma_f32 v74, |v92|, s25, 1.0
	v_fma_f32 v75, |v93|, s25, 1.0
	v_rcp_f32_e32 v74, v74
	v_rcp_f32_e32 v75, v75
	v_pk_mul_f32 v[76:77], v[92:93], v[92:93]
	s_waitcnt vmcnt(0)
	v_add_f32_e32 v101, v232, v233
	v_mul_f32_e32 v76, 0xbf38aa3b, v76
	v_pk_fma_f32 v[78:79], v[74:75], s[22:23], v[90:91] op_sel_hi:[1,0,0]
	v_exp_f32_e32 v96, v76
	v_pk_fma_f32 v[78:79], v[74:75], v[78:79], s[24:25] op_sel_hi:[1,1,0]
	v_add_f32_e32 v76, v208, v209
	v_pk_fma_f32 v[78:79], v[74:75], v[78:79], s[34:35] op_sel_hi:[1,1,0]
	v_mul_f32_e32 v81, 0xbf38aa3b, v77
	v_pk_fma_f32 v[78:79], v[74:75], v[78:79], s[40:41] op_sel_hi:[1,1,0]
	v_add_f32_e32 v77, v212, v213
	v_pk_mul_f32 v[98:99], v[74:75], v[78:79]
	v_add_f32_e32 v74, v202, v203
	v_add_f32_e32 v75, v204, v205
	v_add_f32_e32 v74, v74, v75
	v_add_f32_e32 v75, v206, v207
	v_add_f32_e32 v75, v75, v76
	v_add_f32_e32 v76, v210, v211
	v_add_f32_e32 v76, v76, v77
	v_add_f32_e32 v77, v214, v215
	v_add_f32_e32 v78, v216, v217
	v_add_f32_e32 v77, v77, v78
	v_add_f32_e32 v78, v218, v219
	v_add_f32_e32 v79, v220, v221
	v_add_f32_e32 v78, v78, v79
	v_add_f32_e32 v79, v222, v223
	v_add_f32_e32 v79, v79, v97
	v_add_f32_e32 v97, v226, v227
	v_add_f32_e32 v97, v97, v100
	v_add_f32_e32 v100, v230, v231
	v_add_f32_e32 v100, v100, v101
	v_cndmask_b32_e64 v101, v75, v74, s[4:5]
	v_cndmask_b32_e64 v74, v74, v75, s[4:5]
	v_cndmask_b32_e64 v75, v77, v76, s[4:5]
	v_cndmask_b32_e64 v76, v76, v77, s[4:5]
	v_cndmask_b32_e64 v77, v78, v79, s[4:5]
	v_add_f32_dpp v74, v101, v74 quad_perm:[1,0,3,2] row_mask:0xf bank_mask:0xf bound_ctrl:1
	v_add_f32_dpp v75, v75, v76 quad_perm:[1,0,3,2] row_mask:0xf bank_mask:0xf bound_ctrl:1
	v_cndmask_b32_e64 v76, v79, v78, s[4:5]
	v_cndmask_b32_e64 v78, v97, v100, s[4:5]
	v_and_b32_e32 v95, 0x7fffffff, v93
	v_add_f32_dpp v76, v76, v77 quad_perm:[1,0,3,2] row_mask:0xf bank_mask:0xf bound_ctrl:1
	v_cndmask_b32_e64 v77, v100, v97, s[4:5]
	v_exp_f32_e32 v97, v81
	v_and_b32_e32 v94, 0x7fffffff, v92
	v_add_f32_dpp v77, v77, v78 quad_perm:[1,0,3,2] row_mask:0xf bank_mask:0xf bound_ctrl:1
	v_cndmask_b32_e64 v78, v74, v75, s[6:7]
	v_cndmask_b32_e64 v74, v75, v74, s[6:7]
	v_cndmask_b32_e64 v75, v76, v77, s[6:7]
	v_cndmask_b32_e64 v76, v77, v76, s[6:7]
	v_add_f32_dpp v74, v78, v74 quad_perm:[2,3,0,1] row_mask:0xf bank_mask:0xf bound_ctrl:1
	v_max_f32_e32 v92, 0, v92
	v_add_f32_dpp v75, v75, v76 quad_perm:[2,3,0,1] row_mask:0xf bank_mask:0xf bound_ctrl:1
	v_cndmask_b32_e64 v76, v74, v75, s[8:9]
	v_cndmask_b32_e64 v74, v75, v74, s[8:9]
	v_mov_b32_e32 v75, v76
	v_max_f32_e32 v93, 0, v93
	s_waitcnt lgkmcnt(14)
	v_dot2c_f32_f16_e32 v104, v38, v38
	v_mov_b32_dpp v75, v75 row_shl:4 row_mask:0xf bank_mask:0x5
	v_mov_b32_e32 v105, 0
	v_dot2c_f32_f16_e32 v104, v39, v39
	v_mov_b32_dpp v75, v76 row_shr:4 row_mask:0xf bank_mask:0xa
	v_add_f32_e32 v74, v74, v75
	v_dot2c_f32_f16_e32 v104, v40, v40
	v_dot2c_f32_f16_e32 v104, v41, v41
	v_add_f32_dpp v74, v74, v74 row_ror:8 row_mask:0xf bank_mask:0xf bound_ctrl:1
	v_mov_b32_e32 v75, v74
	s_nop 1
	v_permlane16_swap_b32_e32 v74, v75
	v_add_f32_e32 v74, v74, v75
	v_mov_b32_e32 v75, v74
	s_nop 1
	v_permlane32_swap_b32_e32 v74, v75
	v_add_f32_e32 v74, v74, v75
	v_mul_f32_e32 v74, 0x3b800000, v74
	s_waitcnt lgkmcnt(13)
	v_dot2c_f32_f16_e32 v104, v34, v34
	v_readlane_b32 s42, v74, 0
	v_readlane_b32 s44, v74, 1
	v_readlane_b32 s46, v74, 2
	v_pk_add_f32 v[102:103], v[204:205], s[42:43] op_sel_hi:[1, 0] neg_lo:[0, 1] neg_hi:[0, 1]
	v_pk_add_f32 v[78:79], v[208:209], s[44:45] op_sel_hi:[1, 0] neg_lo:[0, 1] neg_hi:[0, 1]
	v_pk_add_f32 v[100:101], v[202:203], s[42:43] op_sel_hi:[1, 0] neg_lo:[0, 1] neg_hi:[0, 1]
	v_mul_f32_e32 v70, v103, v103
	v_mul_f32_e32 v71, v79, v79
	v_fmac_f32_e32 v70, v102, v102
	v_pk_add_f32 v[86:87], v[206:207], s[44:45] op_sel_hi:[1, 0] neg_lo:[0, 1] neg_hi:[0, 1]
	v_fmac_f32_e32 v71, v78, v78
	v_fmac_f32_e32 v70, v101, v101
	v_fmac_f32_e32 v71, v87, v87
	v_fmac_f32_e32 v70, v100, v100
	v_fmac_f32_e32 v71, v86, v86
	v_readlane_b32 s48, v74, 3
	v_cndmask_b32_e64 v72, v71, v70, s[4:5]
	v_cndmask_b32_e64 v70, v70, v71, s[4:5]
	v_readlane_b32 s50, v74, 4
	v_readlane_b32 s52, v74, 5
	v_readlane_b32 s54, v74, 6
	v_readlane_b32 s0, v74, 7
	v_add_f32_dpp v88, v72, v70 quad_perm:[1,0,3,2] row_mask:0xf bank_mask:0xf bound_ctrl:1
	v_pk_add_f32 v[74:75], v[212:213], s[46:47] op_sel_hi:[1, 0] neg_lo:[0, 1] neg_hi:[0, 1]
	v_pk_add_f32 v[70:71], v[216:217], s[48:49] op_sel_hi:[1, 0] neg_lo:[0, 1] neg_hi:[0, 1]
	v_pk_add_f32 v[76:77], v[210:211], s[46:47] op_sel_hi:[1, 0] neg_lo:[0, 1] neg_hi:[0, 1]
	v_mul_f32_e32 v82, v75, v75
	v_pk_add_f32 v[72:73], v[214:215], s[48:49] op_sel_hi:[1, 0] neg_lo:[0, 1] neg_hi:[0, 1]
	v_mul_f32_e32 v66, v71, v71
	v_fmac_f32_e32 v82, v74, v74
	v_fmac_f32_e32 v66, v70, v70
	v_fmac_f32_e32 v82, v77, v77
	v_fmac_f32_e32 v66, v73, v73
	v_fmac_f32_e32 v82, v76, v76
	v_fmac_f32_e32 v66, v72, v72
	v_cndmask_b32_e64 v67, v66, v82, s[4:5]
	v_cndmask_b32_e64 v66, v82, v66, s[4:5]
	v_pk_add_f32 v[68:69], v[218:219], s[50:51] op_sel_hi:[1, 0] neg_lo:[0, 1] neg_hi:[0, 1]
	v_pk_add_f32 v[62:63], v[222:223], s[52:53] op_sel_hi:[1, 0] neg_lo:[0, 1] neg_hi:[0, 1]
	v_add_f32_dpp v66, v67, v66 quad_perm:[1,0,3,2] row_mask:0xf bank_mask:0xf bound_ctrl:1
	v_cndmask_b32_e64 v67, v88, v66, s[6:7]
	v_cndmask_b32_e64 v66, v66, v88, s[6:7]
	v_pk_add_f32 v[56:57], v[228:229], s[54:55] op_sel_hi:[1, 0] neg_lo:[0, 1] neg_hi:[0, 1]
	v_dot2c_f32_f16_e32 v104, v35, v35
	v_add_f32_dpp v82, v67, v66 quad_perm:[2,3,0,1] row_mask:0xf bank_mask:0xf bound_ctrl:1
	v_pk_add_f32 v[66:67], v[220:221], s[50:51] op_sel_hi:[1, 0] neg_lo:[0, 1] neg_hi:[0, 1]
	v_pk_add_f32 v[60:61], v[224:225], s[52:53] op_sel_hi:[1, 0] neg_lo:[0, 1] neg_hi:[0, 1]
	v_mul_f32_e32 v58, v67, v67
	v_mul_f32_e32 v59, v61, v61
	v_fmac_f32_e32 v58, v66, v66
	v_fmac_f32_e32 v59, v60, v60
	v_fmac_f32_e32 v58, v69, v69
	v_fmac_f32_e32 v59, v63, v63
	v_fmac_f32_e32 v58, v68, v68
	v_fmac_f32_e32 v59, v62, v62
	v_cndmask_b32_e64 v64, v59, v58, s[4:5]
	v_cndmask_b32_e64 v58, v58, v59, s[4:5]
	v_mul_f32_e32 v65, v57, v57
	v_fmac_f32_e32 v65, v56, v56
	v_add_f32_dpp v64, v64, v58 quad_perm:[1,0,3,2] row_mask:0xf bank_mask:0xf bound_ctrl:1
	v_pk_add_f32 v[58:59], v[226:227], s[54:55] op_sel_hi:[1, 0] neg_lo:[0, 1] neg_hi:[0, 1]
	v_pk_add_f32 v[54:55], v[230:231], s[0:1] op_sel_hi:[1, 0] neg_lo:[0, 1] neg_hi:[0, 1]
	v_pk_add_f32 v[50:51], v[232:233], s[0:1] op_sel_hi:[1, 0] neg_lo:[0, 1] neg_hi:[0, 1]
	v_fmac_f32_e32 v65, v59, v59
	v_mul_f32_e32 v52, v51, v51
	v_fmac_f32_e32 v52, v50, v50
	v_fmac_f32_e32 v52, v55, v55
	v_fmac_f32_e32 v65, v58, v58
	v_fmac_f32_e32 v52, v54, v54
	v_cndmask_b32_e64 v53, v52, v65, s[4:5]
	v_cndmask_b32_e64 v52, v65, v52, s[4:5]
	v_dot2c_f32_f16_e32 v104, v36, v36
	v_dot2c_f32_f16_e32 v104, v37, v37
	v_add_f32_dpp v52, v53, v52 quad_perm:[1,0,3,2] row_mask:0xf bank_mask:0xf bound_ctrl:1
	v_cndmask_b32_e64 v53, v64, v52, s[6:7]
	v_cndmask_b32_e64 v52, v52, v64, s[6:7]
	s_waitcnt lgkmcnt(12)
	v_dot2c_f32_f16_e32 v104, v30, v30
	v_dot2c_f32_f16_e32 v104, v31, v31
	v_add_f32_dpp v52, v53, v52 quad_perm:[2,3,0,1] row_mask:0xf bank_mask:0xf bound_ctrl:1
	v_cndmask_b32_e64 v53, v82, v52, s[8:9]
	v_mov_b32_e32 v64, v53
	v_cndmask_b32_e64 v52, v52, v82, s[8:9]
	v_dot2c_f32_f16_e32 v104, v32, v32
	v_mov_b32_dpp v64, v64 row_shl:4 row_mask:0xf bank_mask:0x5
	v_dot2c_f32_f16_e32 v104, v33, v33
	s_waitcnt lgkmcnt(11)
	v_dot2c_f32_f16_e32 v104, v26, v26
	v_mov_b32_dpp v64, v53 row_shr:4 row_mask:0xf bank_mask:0xa
	v_add_f32_e32 v52, v52, v64
	v_dot2c_f32_f16_e32 v104, v27, v27
	v_dot2c_f32_f16_e32 v104, v28, v28
	v_add_f32_dpp v52, v52, v52 row_ror:8 row_mask:0xf bank_mask:0xf bound_ctrl:1
	v_mov_b32_e32 v53, v52
	s_nop 1
	v_permlane16_swap_b32_e32 v52, v53
	v_add_f32_e32 v52, v52, v53
	v_mov_b32_e32 v53, v52
	s_nop 1
	v_permlane32_swap_b32_e32 v52, v53
	v_add_f32_e32 v52, v52, v53
	v_fmac_f32_e32 v116, 0x3b800000, v52
	v_mul_f32_e32 v52, 0x4f800000, v116
	v_cmp_gt_f32_e32 vcc, s35, v116
	v_dot2c_f32_f16_e32 v104, v29, v29
	s_waitcnt lgkmcnt(10)
	v_dot2c_f32_f16_e32 v104, v22, v22
	v_cndmask_b32_e32 v64, v116, v52, vcc
	v_sqrt_f32_e32 v65, v64
	v_pk_mul_f32 v[52:53], v[94:95], v[98:99]
	v_and_b32_e32 v94, 48, v0
	v_pk_fma_f32 v[52:53], v[96:97], v[52:53], v[92:93] neg_lo:[1,0,0] neg_hi:[1,0,0]
	v_add_u32_e32 v81, -1, v65
	v_fma_f32 v82, -v81, v65, v64
	v_cmp_ge_f32_e64 s[0:1], 0, v82
	v_add_u32_e32 v82, 1, v65
	v_add_u32_e32 v95, 0x19860, v94
	v_cndmask_b32_e64 v81, v65, v81, s[0:1]
	v_fma_f32 v65, -v82, v65, v64
	v_cmp_lt_f32_e64 s[0:1], 0, v65
	v_dot2c_f32_f16_e32 v104, v23, v23
	v_dot2c_f32_f16_e32 v104, v24, v24
	v_cndmask_b32_e64 v65, v81, v82, s[0:1]
	v_mul_f32_e32 v81, 0x37800000, v65
	v_cndmask_b32_e32 v65, v65, v81, vcc
	v_cmp_class_f32_e32 vcc, v64, v117
	v_cvt_pk_f16_f32 v81, v52, v53
	ds_write_b64 v144, v[80:81] offset:36352
	v_cndmask_b32_e32 v64, v65, v64, vcc
	v_div_scale_f32 v65, s[0:1], v64, v64, 1.0
	v_rcp_f32_e32 v82, v65
	v_dot2c_f32_f16_e32 v104, v25, v25
	s_waitcnt lgkmcnt(10)
	v_dot2c_f32_f16_e32 v104, v18, v18
	v_dot2c_f32_f16_e32 v104, v19, v19
	v_fma_f32 v52, -v65, v82, 1.0
	v_fmac_f32_e32 v82, v52, v82
	v_div_scale_f32 v52, vcc, 1.0, v64, 1.0
	v_mul_f32_e32 v53, v52, v82
	v_fma_f32 v80, -v65, v53, v52
	v_fmac_f32_e32 v53, v80, v82
	v_fma_f32 v52, -v65, v53, v52
	v_div_fmas_f32 v52, v52, v82, v53
	v_div_fixup_f32 v52, v52, v64, 1.0
	v_dot2c_f32_f16_e32 v104, v20, v20
	v_readlane_b32 s0, v52, 0
	v_dot2c_f32_f16_e32 v104, v21, v21
	s_waitcnt lgkmcnt(9)
	v_dot2c_f32_f16_e32 v104, v14, v14
	v_pk_mul_f32 v[64:65], s[0:1], v[100:101] op_sel_hi:[0,1]
	v_pk_fma_f32 v[64:65], v[64:65], v[238:239], v[242:243]
	v_dot2c_f32_f16_e32 v104, v15, v15
	v_fma_f32 v53, |v64|, s25, 1.0
	v_rcp_f32_e32 v82, v53
	v_fma_f32 v53, |v65|, s25, 1.0
	v_rcp_f32_e32 v83, v53
	v_pk_mul_f32 v[84:85], v[64:65], v[64:65]
	v_and_b32_e32 v81, 0x7fffffff, v65
	v_mul_f32_e32 v53, 0xbf38aa3b, v84
	v_pk_fma_f32 v[88:89], v[82:83], s[22:23], v[90:91] op_sel_hi:[1,0,0]
	v_exp_f32_e32 v84, v53
	v_pk_fma_f32 v[88:89], v[82:83], v[88:89], s[24:25] op_sel_hi:[1,1,0]
	v_mul_f32_e32 v53, 0xbf38aa3b, v85
	v_pk_fma_f32 v[88:89], v[82:83], v[88:89], s[34:35] op_sel_hi:[1,1,0]
	v_exp_f32_e32 v85, v53
	v_pk_fma_f32 v[88:89], v[82:83], v[88:89], s[40:41] op_sel_hi:[1,1,0]
	v_and_b32_e32 v80, 0x7fffffff, v64
	v_pk_mul_f32 v[82:83], v[82:83], v[88:89]
	v_max_f32_e32 v64, 0, v64
	v_max_f32_e32 v65, 0, v65
	v_pk_mul_f32 v[80:81], v[80:81], v[82:83]
	v_dot2c_f32_f16_e32 v104, v16, v16
	v_pk_fma_f32 v[64:65], v[84:85], v[80:81], v[64:65] neg_lo:[1,0,0] neg_hi:[1,0,0]
	v_pk_mul_f32 v[80:81], s[0:1], v[102:103] op_sel_hi:[0,1]
	v_pk_fma_f32 v[80:81], v[80:81], v[240:241], v[244:245]
	v_cvt_pk_f16_f32 v64, v64, v65
	v_fma_f32 v53, |v80|, s25, 1.0
	v_rcp_f32_e32 v84, v53
	v_fma_f32 v53, |v81|, s25, 1.0
	v_rcp_f32_e32 v85, v53
	v_pk_mul_f32 v[88:89], v[80:81], v[80:81]
	v_and_b32_e32 v83, 0x7fffffff, v81
	v_mul_f32_e32 v53, 0xbf38aa3b, v88
	v_pk_fma_f32 v[92:93], v[84:85], s[22:23], v[90:91] op_sel_hi:[1,0,0]
	v_exp_f32_e32 v88, v53
	v_pk_fma_f32 v[92:93], v[84:85], v[92:93], s[24:25] op_sel_hi:[1,1,0]
	v_mul_f32_e32 v53, 0xbf38aa3b, v89
	v_pk_fma_f32 v[92:93], v[84:85], v[92:93], s[34:35] op_sel_hi:[1,1,0]
	v_exp_f32_e32 v89, v53
	v_pk_fma_f32 v[92:93], v[84:85], v[92:93], s[40:41] op_sel_hi:[1,1,0]
	v_and_b32_e32 v82, 0x7fffffff, v80
	v_pk_mul_f32 v[84:85], v[84:85], v[92:93]
	v_max_f32_e32 v80, 0, v80
	v_max_f32_e32 v81, 0, v81
	v_pk_mul_f32 v[82:83], v[82:83], v[84:85]
	v_readlane_b32 s0, v52, 1
	v_pk_fma_f32 v[80:81], v[88:89], v[82:83], v[80:81] neg_lo:[1,0,0] neg_hi:[1,0,0]
	v_dot2c_f32_f16_e32 v104, v17, v17
	v_cvt_pk_f16_f32 v65, v80, v81
	ds_write_b64 v145, v[64:65] offset:36864
	v_pk_mul_f32 v[64:65], s[0:1], v[86:87] op_sel_hi:[0,1]
	v_pk_fma_f32 v[64:65], v[64:65], v[238:239], v[242:243]
	v_pk_mul_f32 v[78:79], s[0:1], v[78:79] op_sel_hi:[0,1]
	v_fma_f32 v53, |v64|, s25, 1.0
	v_rcp_f32_e32 v82, v53
	v_fma_f32 v53, |v65|, s25, 1.0
	v_rcp_f32_e32 v83, v53
	v_pk_mul_f32 v[84:85], v[64:65], v[64:65]
	v_pk_fma_f32 v[78:79], v[78:79], v[240:241], v[244:245]
	v_mul_f32_e32 v53, 0xbf38aa3b, v84
	v_pk_fma_f32 v[86:87], v[82:83], s[22:23], v[90:91] op_sel_hi:[1,0,0]
	v_exp_f32_e32 v84, v53
	v_pk_fma_f32 v[86:87], v[82:83], v[86:87], s[24:25] op_sel_hi:[1,1,0]
	v_mul_f32_e32 v53, 0xbf38aa3b, v85
	v_pk_fma_f32 v[86:87], v[82:83], v[86:87], s[34:35] op_sel_hi:[1,1,0]
	v_and_b32_e32 v81, 0x7fffffff, v65
	v_pk_fma_f32 v[86:87], v[82:83], v[86:87], s[40:41] op_sel_hi:[1,1,0]
	v_and_b32_e32 v80, 0x7fffffff, v64
	v_exp_f32_e32 v85, v53
	v_pk_mul_f32 v[82:83], v[82:83], v[86:87]
	v_fma_f32 v53, |v78|, s25, 1.0
	v_pk_mul_f32 v[80:81], v[80:81], v[82:83]
	v_rcp_f32_e32 v82, v53
	v_fma_f32 v53, |v79|, s25, 1.0
	v_rcp_f32_e32 v83, v53
	v_max_f32_e32 v64, 0, v64
	v_max_f32_e32 v65, 0, v65
	v_pk_fma_f32 v[64:65], v[84:85], v[80:81], v[64:65] neg_lo:[1,0,0] neg_hi:[1,0,0]
	v_pk_mul_f32 v[84:85], v[78:79], v[78:79]
	v_pk_fma_f32 v[86:87], v[82:83], s[22:23], v[90:91] op_sel_hi:[1,0,0]
	v_mul_f32_e32 v53, 0xbf38aa3b, v84
	v_exp_f32_e32 v84, v53
	v_pk_fma_f32 v[86:87], v[82:83], v[86:87], s[24:25] op_sel_hi:[1,1,0]
	v_mul_f32_e32 v53, 0xbf38aa3b, v85
	v_pk_fma_f32 v[86:87], v[82:83], v[86:87], s[34:35] op_sel_hi:[1,1,0]
	v_exp_f32_e32 v85, v53
	v_pk_fma_f32 v[86:87], v[82:83], v[86:87], s[40:41] op_sel_hi:[1,1,0]
	v_and_b32_e32 v81, 0x7fffffff, v79
	v_and_b32_e32 v80, 0x7fffffff, v78
	v_pk_mul_f32 v[82:83], v[82:83], v[86:87]
	v_max_f32_e32 v78, 0, v78
	v_max_f32_e32 v79, 0, v79
	v_pk_mul_f32 v[80:81], v[80:81], v[82:83]
	v_cvt_pk_f16_f32 v64, v64, v65
	v_pk_fma_f32 v[78:79], v[84:85], v[80:81], v[78:79] neg_lo:[1,0,0] neg_hi:[1,0,0]
	v_readlane_b32 s0, v52, 2
	v_cvt_pk_f16_f32 v65, v78, v79
	ds_write_b64 v139, v[64:65] offset:37376
	v_pk_mul_f32 v[64:65], s[0:1], v[76:77] op_sel_hi:[0,1]
	v_pk_fma_f32 v[64:65], v[64:65], v[238:239], v[242:243]
	v_pk_mul_f32 v[74:75], s[0:1], v[74:75] op_sel_hi:[0,1]
	v_fma_f32 v53, |v64|, s25, 1.0
	v_rcp_f32_e32 v78, v53
	v_fma_f32 v53, |v65|, s25, 1.0
	v_rcp_f32_e32 v79, v53
	v_pk_mul_f32 v[80:81], v[64:65], v[64:65]
	v_pk_fma_f32 v[74:75], v[74:75], v[240:241], v[244:245]
	v_mul_f32_e32 v53, 0xbf38aa3b, v80
	v_pk_fma_f32 v[82:83], v[78:79], s[22:23], v[90:91] op_sel_hi:[1,0,0]
	v_exp_f32_e32 v80, v53
	v_pk_fma_f32 v[82:83], v[78:79], v[82:83], s[24:25] op_sel_hi:[1,1,0]
	v_mul_f32_e32 v53, 0xbf38aa3b, v81
	v_pk_fma_f32 v[82:83], v[78:79], v[82:83], s[34:35] op_sel_hi:[1,1,0]
	v_and_b32_e32 v77, 0x7fffffff, v65
	v_pk_fma_f32 v[82:83], v[78:79], v[82:83], s[40:41] op_sel_hi:[1,1,0]
	v_and_b32_e32 v76, 0x7fffffff, v64
	v_exp_f32_e32 v81, v53
	v_pk_mul_f32 v[78:79], v[78:79], v[82:83]
	v_fma_f32 v53, |v74|, s25, 1.0
	v_pk_mul_f32 v[76:77], v[76:77], v[78:79]
	v_rcp_f32_e32 v78, v53
	v_fma_f32 v53, |v75|, s25, 1.0
	v_rcp_f32_e32 v79, v53
	v_max_f32_e32 v64, 0, v64
	v_max_f32_e32 v65, 0, v65
	v_pk_fma_f32 v[64:65], v[80:81], v[76:77], v[64:65] neg_lo:[1,0,0] neg_hi:[1,0,0]
	v_pk_mul_f32 v[80:81], v[74:75], v[74:75]
	v_pk_fma_f32 v[82:83], v[78:79], s[22:23], v[90:91] op_sel_hi:[1,0,0]
	v_mul_f32_e32 v53, 0xbf38aa3b, v80
	v_exp_f32_e32 v80, v53
	v_pk_fma_f32 v[82:83], v[78:79], v[82:83], s[24:25] op_sel_hi:[1,1,0]
	v_mul_f32_e32 v53, 0xbf38aa3b, v81
	v_pk_fma_f32 v[82:83], v[78:79], v[82:83], s[34:35] op_sel_hi:[1,1,0]
	v_exp_f32_e32 v81, v53
	v_pk_fma_f32 v[82:83], v[78:79], v[82:83], s[40:41] op_sel_hi:[1,1,0]
	v_and_b32_e32 v77, 0x7fffffff, v75
	v_and_b32_e32 v76, 0x7fffffff, v74
	v_pk_mul_f32 v[78:79], v[78:79], v[82:83]
	v_max_f32_e32 v74, 0, v74
	v_max_f32_e32 v75, 0, v75
	v_pk_mul_f32 v[76:77], v[76:77], v[78:79]
	v_cvt_pk_f16_f32 v64, v64, v65
	v_pk_fma_f32 v[74:75], v[80:81], v[76:77], v[74:75] neg_lo:[1,0,0] neg_hi:[1,0,0]
	v_readlane_b32 s0, v52, 3
	v_cvt_pk_f16_f32 v65, v74, v75
	ds_write_b64 v137, v[64:65] offset:37888
	v_pk_mul_f32 v[64:65], s[0:1], v[72:73] op_sel_hi:[0,1]
	v_pk_fma_f32 v[64:65], v[64:65], v[238:239], v[242:243]
	v_pk_mul_f32 v[70:71], s[0:1], v[70:71] op_sel_hi:[0,1]
	v_fma_f32 v53, |v64|, s25, 1.0
	v_rcp_f32_e32 v74, v53
	v_fma_f32 v53, |v65|, s25, 1.0
	v_rcp_f32_e32 v75, v53
	v_pk_mul_f32 v[76:77], v[64:65], v[64:65]
	v_pk_fma_f32 v[70:71], v[70:71], v[240:241], v[244:245]
	v_mul_f32_e32 v53, 0xbf38aa3b, v76
	v_pk_fma_f32 v[78:79], v[74:75], s[22:23], v[90:91] op_sel_hi:[1,0,0]
	v_exp_f32_e32 v76, v53
	v_pk_fma_f32 v[78:79], v[74:75], v[78:79], s[24:25] op_sel_hi:[1,1,0]
	v_mul_f32_e32 v53, 0xbf38aa3b, v77
	v_pk_fma_f32 v[78:79], v[74:75], v[78:79], s[34:35] op_sel_hi:[1,1,0]
	v_and_b32_e32 v73, 0x7fffffff, v65
	v_pk_fma_f32 v[78:79], v[74:75], v[78:79], s[40:41] op_sel_hi:[1,1,0]
	v_and_b32_e32 v72, 0x7fffffff, v64
	v_exp_f32_e32 v77, v53
	v_pk_mul_f32 v[74:75], v[74:75], v[78:79]
	v_fma_f32 v53, |v70|, s25, 1.0
	v_pk_mul_f32 v[72:73], v[72:73], v[74:75]
	v_rcp_f32_e32 v74, v53
	v_fma_f32 v53, |v71|, s25, 1.0
	v_rcp_f32_e32 v75, v53
	v_max_f32_e32 v64, 0, v64
	v_max_f32_e32 v65, 0, v65
	v_pk_fma_f32 v[64:65], v[76:77], v[72:73], v[64:65] neg_lo:[1,0,0] neg_hi:[1,0,0]
	v_pk_mul_f32 v[76:77], v[70:71], v[70:71]
	v_pk_fma_f32 v[78:79], v[74:75], s[22:23], v[90:91] op_sel_hi:[1,0,0]
	v_mul_f32_e32 v53, 0xbf38aa3b, v76
	v_exp_f32_e32 v76, v53
	v_pk_fma_f32 v[78:79], v[74:75], v[78:79], s[24:25] op_sel_hi:[1,1,0]
	v_mul_f32_e32 v53, 0xbf38aa3b, v77
	v_pk_fma_f32 v[78:79], v[74:75], v[78:79], s[34:35] op_sel_hi:[1,1,0]
	v_exp_f32_e32 v77, v53
	v_pk_fma_f32 v[78:79], v[74:75], v[78:79], s[40:41] op_sel_hi:[1,1,0]
	v_and_b32_e32 v73, 0x7fffffff, v71
	v_and_b32_e32 v72, 0x7fffffff, v70
	v_pk_mul_f32 v[74:75], v[74:75], v[78:79]
	v_max_f32_e32 v70, 0, v70
	v_max_f32_e32 v71, 0, v71
	v_pk_mul_f32 v[72:73], v[72:73], v[74:75]
	v_cvt_pk_f16_f32 v64, v64, v65
	v_pk_fma_f32 v[70:71], v[76:77], v[72:73], v[70:71] neg_lo:[1,0,0] neg_hi:[1,0,0]
	v_readlane_b32 s0, v52, 4
	v_cvt_pk_f16_f32 v65, v70, v71
	ds_write_b64 v136, v[64:65] offset:38400
	v_pk_mul_f32 v[64:65], s[0:1], v[68:69] op_sel_hi:[0,1]
	v_pk_fma_f32 v[64:65], v[64:65], v[238:239], v[242:243]
	v_pk_mul_f32 v[66:67], s[0:1], v[66:67] op_sel_hi:[0,1]
	v_fma_f32 v53, |v64|, s25, 1.0
	v_rcp_f32_e32 v70, v53
	v_fma_f32 v53, |v65|, s25, 1.0
	v_rcp_f32_e32 v71, v53
	v_pk_mul_f32 v[72:73], v[64:65], v[64:65]
	v_pk_fma_f32 v[66:67], v[66:67], v[240:241], v[244:245]
	v_mul_f32_e32 v53, 0xbf38aa3b, v72
	v_pk_fma_f32 v[74:75], v[70:71], s[22:23], v[90:91] op_sel_hi:[1,0,0]
	v_exp_f32_e32 v72, v53
	v_pk_fma_f32 v[74:75], v[70:71], v[74:75], s[24:25] op_sel_hi:[1,1,0]
	v_mul_f32_e32 v53, 0xbf38aa3b, v73
	v_pk_fma_f32 v[74:75], v[70:71], v[74:75], s[34:35] op_sel_hi:[1,1,0]
	v_and_b32_e32 v69, 0x7fffffff, v65
	v_pk_fma_f32 v[74:75], v[70:71], v[74:75], s[40:41] op_sel_hi:[1,1,0]
	v_and_b32_e32 v68, 0x7fffffff, v64
	v_exp_f32_e32 v73, v53
	v_pk_mul_f32 v[70:71], v[70:71], v[74:75]
	v_fma_f32 v53, |v66|, s25, 1.0
	v_pk_mul_f32 v[68:69], v[68:69], v[70:71]
	v_rcp_f32_e32 v70, v53
	v_fma_f32 v53, |v67|, s25, 1.0
	v_rcp_f32_e32 v71, v53
	v_max_f32_e32 v64, 0, v64
	v_max_f32_e32 v65, 0, v65
	v_pk_fma_f32 v[64:65], v[72:73], v[68:69], v[64:65] neg_lo:[1,0,0] neg_hi:[1,0,0]
	v_pk_mul_f32 v[72:73], v[66:67], v[66:67]
	v_pk_fma_f32 v[74:75], v[70:71], s[22:23], v[90:91] op_sel_hi:[1,0,0]
	v_mul_f32_e32 v53, 0xbf38aa3b, v72
	v_exp_f32_e32 v72, v53
	v_pk_fma_f32 v[74:75], v[70:71], v[74:75], s[24:25] op_sel_hi:[1,1,0]
	v_mul_f32_e32 v53, 0xbf38aa3b, v73
	v_pk_fma_f32 v[74:75], v[70:71], v[74:75], s[34:35] op_sel_hi:[1,1,0]
	v_exp_f32_e32 v73, v53
	v_pk_fma_f32 v[74:75], v[70:71], v[74:75], s[40:41] op_sel_hi:[1,1,0]
	v_readlane_b32 s0, v52, 5
	v_and_b32_e32 v69, 0x7fffffff, v67
	v_and_b32_e32 v68, 0x7fffffff, v66
	v_pk_mul_f32 v[70:71], v[70:71], v[74:75]
	v_pk_mul_f32 v[62:63], s[0:1], v[62:63] op_sel_hi:[0,1]
	v_max_f32_e32 v66, 0, v66
	v_max_f32_e32 v67, 0, v67
	v_pk_mul_f32 v[68:69], v[68:69], v[70:71]
	v_pk_fma_f32 v[62:63], v[62:63], v[238:239], v[242:243]
	v_pk_fma_f32 v[66:67], v[72:73], v[68:69], v[66:67] neg_lo:[1,0,0] neg_hi:[1,0,0]
	v_fma_f32 v53, |v62|, s25, 1.0
	v_cvt_pk_f16_f32 v64, v64, v65
	v_cvt_pk_f16_f32 v65, v66, v67
	v_rcp_f32_e32 v66, v53
	v_fma_f32 v53, |v63|, s25, 1.0
	v_rcp_f32_e32 v67, v53
	v_pk_mul_f32 v[68:69], v[62:63], v[62:63]
	v_pk_mul_f32 v[60:61], s[0:1], v[60:61] op_sel_hi:[0,1]
	v_mul_f32_e32 v53, 0xbf38aa3b, v68
	v_pk_fma_f32 v[70:71], v[66:67], s[22:23], v[90:91] op_sel_hi:[1,0,0]
	v_exp_f32_e32 v68, v53
	v_pk_fma_f32 v[70:71], v[66:67], v[70:71], s[24:25] op_sel_hi:[1,1,0]
	v_mul_f32_e32 v53, 0xbf38aa3b, v69
	v_pk_fma_f32 v[70:71], v[66:67], v[70:71], s[34:35] op_sel_hi:[1,1,0]
	v_pk_fma_f32 v[60:61], v[60:61], v[240:241], v[244:245]
	v_pk_fma_f32 v[70:71], v[66:67], v[70:71], s[40:41] op_sel_hi:[1,1,0]
	ds_write_b64 v123, v[64:65] offset:38912
	v_and_b32_e32 v65, 0x7fffffff, v63
	v_and_b32_e32 v64, 0x7fffffff, v62
	v_exp_f32_e32 v69, v53
	v_pk_mul_f32 v[66:67], v[66:67], v[70:71]
	v_fma_f32 v53, |v60|, s25, 1.0
	v_pk_mul_f32 v[64:65], v[64:65], v[66:67]
	v_rcp_f32_e32 v66, v53
	v_fma_f32 v53, |v61|, s25, 1.0
	v_rcp_f32_e32 v67, v53
	v_max_f32_e32 v62, 0, v62
	v_max_f32_e32 v63, 0, v63
	v_pk_fma_f32 v[62:63], v[68:69], v[64:65], v[62:63] neg_lo:[1,0,0] neg_hi:[1,0,0]
	v_pk_mul_f32 v[68:69], v[60:61], v[60:61]
	v_pk_fma_f32 v[70:71], v[66:67], s[22:23], v[90:91] op_sel_hi:[1,0,0]
	v_mul_f32_e32 v53, 0xbf38aa3b, v68
	v_exp_f32_e32 v68, v53
	v_pk_fma_f32 v[70:71], v[66:67], v[70:71], s[24:25] op_sel_hi:[1,1,0]
	v_mul_f32_e32 v53, 0xbf38aa3b, v69
	v_pk_fma_f32 v[70:71], v[66:67], v[70:71], s[34:35] op_sel_hi:[1,1,0]
	v_exp_f32_e32 v69, v53
	v_pk_fma_f32 v[70:71], v[66:67], v[70:71], s[40:41] op_sel_hi:[1,1,0]
	v_and_b32_e32 v65, 0x7fffffff, v61
	v_and_b32_e32 v64, 0x7fffffff, v60
	v_pk_mul_f32 v[66:67], v[66:67], v[70:71]
	v_readlane_b32 s0, v52, 6
	v_max_f32_e32 v60, 0, v60
	v_max_f32_e32 v61, 0, v61
	v_pk_mul_f32 v[64:65], v[64:65], v[66:67]
	v_pk_mul_f32 v[58:59], s[0:1], v[58:59] op_sel_hi:[0,1]
	v_pk_fma_f32 v[60:61], v[68:69], v[64:65], v[60:61] neg_lo:[1,0,0] neg_hi:[1,0,0]
	v_pk_fma_f32 v[58:59], v[58:59], v[238:239], v[242:243]
	v_cvt_pk_f16_f32 v62, v62, v63
	v_cvt_pk_f16_f32 v63, v60, v61
	v_fma_f32 v53, |v58|, s25, 1.0
	ds_write_b64 v133, v[62:63] offset:39424
	v_rcp_f32_e32 v62, v53
	v_fma_f32 v53, |v59|, s25, 1.0
	v_rcp_f32_e32 v63, v53
	v_pk_mul_f32 v[64:65], v[58:59], v[58:59]
	v_pk_mul_f32 v[56:57], s[0:1], v[56:57] op_sel_hi:[0,1]
	v_mul_f32_e32 v53, 0xbf38aa3b, v64
	v_pk_fma_f32 v[66:67], v[62:63], s[22:23], v[90:91] op_sel_hi:[1,0,0]
	v_exp_f32_e32 v64, v53
	v_pk_fma_f32 v[66:67], v[62:63], v[66:67], s[24:25] op_sel_hi:[1,1,0]
	v_mul_f32_e32 v53, 0xbf38aa3b, v65
	v_pk_fma_f32 v[66:67], v[62:63], v[66:67], s[34:35] op_sel_hi:[1,1,0]
	v_exp_f32_e32 v65, v53
	v_pk_fma_f32 v[66:67], v[62:63], v[66:67], s[40:41] op_sel_hi:[1,1,0]
	v_pk_fma_f32 v[56:57], v[56:57], v[240:241], v[244:245]
	v_and_b32_e32 v61, 0x7fffffff, v59
	v_and_b32_e32 v60, 0x7fffffff, v58
	v_pk_mul_f32 v[62:63], v[62:63], v[66:67]
	v_fma_f32 v53, |v56|, s25, 1.0
	v_pk_mul_f32 v[60:61], v[60:61], v[62:63]
	v_rcp_f32_e32 v62, v53
	v_fma_f32 v53, |v57|, s25, 1.0
	v_max_f32_e32 v58, 0, v58
	v_max_f32_e32 v59, 0, v59
	v_rcp_f32_e32 v63, v53
	v_pk_fma_f32 v[58:59], v[64:65], v[60:61], v[58:59] neg_lo:[1,0,0] neg_hi:[1,0,0]
	v_pk_mul_f32 v[64:65], v[56:57], v[56:57]
	v_readlane_b32 s0, v52, 7
	v_mul_f32_e32 v53, 0xbf38aa3b, v64
	v_exp_f32_e32 v64, v53
	v_mul_f32_e32 v53, 0xbf38aa3b, v65
	v_pk_fma_f32 v[66:67], v[62:63], s[22:23], v[90:91] op_sel_hi:[1,0,0]
	v_exp_f32_e32 v65, v53
	v_pk_mul_f32 v[52:53], s[0:1], v[54:55] op_sel_hi:[0,1]
	v_pk_fma_f32 v[66:67], v[62:63], v[66:67], s[24:25] op_sel_hi:[1,1,0]
	v_pk_fma_f32 v[42:43], v[52:53], v[238:239], v[242:243]
	v_pk_fma_f32 v[66:67], v[62:63], v[66:67], s[34:35] op_sel_hi:[1,1,0]
	v_fma_f32 v52, |v42|, s25, 1.0
	v_fma_f32 v53, |v43|, s25, 1.0
	v_pk_fma_f32 v[66:67], v[62:63], v[66:67], s[40:41] op_sel_hi:[1,1,0]
	v_rcp_f32_e32 v52, v52
	v_rcp_f32_e32 v53, v53
	v_and_b32_e32 v61, 0x7fffffff, v57
	v_and_b32_e32 v60, 0x7fffffff, v56
	v_pk_mul_f32 v[62:63], v[62:63], v[66:67]
	v_max_f32_e32 v56, 0, v56
	v_max_f32_e32 v57, 0, v57
	v_pk_mul_f32 v[60:61], v[60:61], v[62:63]
	v_cvt_pk_f16_f32 v58, v58, v59
	v_pk_fma_f32 v[56:57], v[64:65], v[60:61], v[56:57] neg_lo:[1,0,0] neg_hi:[1,0,0]
	v_pk_mul_f32 v[54:55], v[42:43], v[42:43]
	v_cvt_pk_f16_f32 v59, v56, v57
	v_pk_fma_f32 v[56:57], v[52:53], s[22:23], v[90:91] op_sel_hi:[1,0,0]
	v_mul_f32_e32 v54, 0xbf38aa3b, v54
	v_pk_fma_f32 v[56:57], v[52:53], v[56:57], s[24:25] op_sel_hi:[1,1,0]
	v_mul_f32_e32 v55, 0xbf38aa3b, v55
	v_exp_f32_e32 v54, v54
	v_pk_fma_f32 v[56:57], v[52:53], v[56:57], s[34:35] op_sel_hi:[1,1,0]
	v_exp_f32_e32 v55, v55
	v_pk_fma_f32 v[56:57], v[52:53], v[56:57], s[40:41] op_sel_hi:[1,1,0]
	v_and_b32_e32 v47, 0x7fffffff, v43
	v_and_b32_e32 v46, 0x7fffffff, v42
	v_pk_mul_f32 v[52:53], v[52:53], v[56:57]
	v_max_f32_e32 v42, 0, v42
	v_max_f32_e32 v43, 0, v43
	v_pk_mul_f32 v[46:47], v[46:47], v[52:53]
	ds_write_b64 v119, v[58:59] offset:39936
	v_pk_fma_f32 v[42:43], v[54:55], v[46:47], v[42:43] neg_lo:[1,0,0] neg_hi:[1,0,0]
	v_pk_mul_f32 v[46:47], s[0:1], v[50:51] op_sel_hi:[0,1]
	v_pk_fma_f32 v[44:45], v[46:47], v[240:241], v[244:245]
	v_cvt_pk_f16_f32 v42, v42, v43
	v_fma_f32 v43, |v44|, s25, 1.0
	v_rcp_f32_e32 v48, v43
	v_fma_f32 v43, |v45|, s25, 1.0
	v_rcp_f32_e32 v49, v43
	v_pk_mul_f32 v[50:51], v[44:45], v[44:45]
	v_and_b32_e32 v47, 0x7fffffff, v45
	v_mul_f32_e32 v43, 0xbf38aa3b, v50
	v_pk_fma_f32 v[52:53], v[48:49], s[22:23], v[90:91] op_sel_hi:[1,0,0]
	v_exp_f32_e32 v50, v43
	v_pk_fma_f32 v[52:53], v[48:49], v[52:53], s[24:25] op_sel_hi:[1,1,0]
	v_mul_f32_e32 v43, 0xbf38aa3b, v51
	v_pk_fma_f32 v[52:53], v[48:49], v[52:53], s[34:35] op_sel_hi:[1,1,0]
	v_exp_f32_e32 v51, v43
	v_pk_fma_f32 v[52:53], v[48:49], v[52:53], s[40:41] op_sel_hi:[1,1,0]
	v_and_b32_e32 v46, 0x7fffffff, v44
	v_pk_mul_f32 v[48:49], v[48:49], v[52:53]
	v_max_f32_e32 v44, 0, v44
	v_max_f32_e32 v45, 0, v45
	v_pk_mul_f32 v[46:47], v[46:47], v[48:49]
	s_waitcnt lgkmcnt(14)
	v_dot2c_f32_f16_e32 v104, v10, v10
	v_pk_fma_f32 v[44:45], v[50:51], v[46:47], v[44:45] neg_lo:[1,0,0] neg_hi:[1,0,0]
	v_dot2c_f32_f16_e32 v104, v11, v11
	v_cvt_pk_f16_f32 v43, v44, v45
	ds_write_b64 v146, v[42:43] offset:40448
	ds_read_b128 v[70:73], v115 offset:32768
	ds_read_b128 v[66:69], v147 offset:32768
	ds_read_b128 v[62:65], v148 offset:32768
	ds_read_b128 v[58:61], v149 offset:32768
	ds_read_b128 v[54:57], v150 offset:33024
	ds_read_b128 v[50:53], v151 offset:33024
	ds_read_b128 v[46:49], v152 offset:33024
	ds_read_b128 v[42:45], v153 offset:33024
	ds_read_b128 v[74:77], v95
	ds_read_b128 v[78:81], v95 offset:64
	ds_read_b128 v[82:85], v95 offset:128
	ds_read_b128 v[86:89], v95 offset:192
	ds_read_b128 v[90:93], v95 offset:256
	ds_read_b128 v[96:99], v95 offset:320
	s_waitcnt lgkmcnt(5)
	v_dot2c_f32_f16_e32 v105, v38, v74
	v_dot2c_f32_f16_e32 v105, v39, v75
	ds_read_b128 v[100:103], v95 offset:384
	ds_read_b128 v[108:111], v95 offset:448
	v_mov_b32_e32 v95, 0
	v_dot2c_f32_f16_e32 v105, v40, v76
	v_dot2c_f32_f16_e32 v95, v70, v70
	v_dot2c_f32_f16_e32 v105, v41, v77
	v_mov_b32_e32 v115, 0
	v_dot2c_f32_f16_e32 v95, v71, v71
	s_waitcnt lgkmcnt(6)
	v_dot2c_f32_f16_e32 v105, v34, v78
	v_dot2c_f32_f16_e32 v115, v70, v74
	v_dot2c_f32_f16_e32 v95, v72, v72
	v_dot2c_f32_f16_e32 v105, v35, v79
	v_dot2c_f32_f16_e32 v115, v71, v75
	v_dot2c_f32_f16_e32 v95, v73, v73
	v_dot2c_f32_f16_e32 v105, v36, v80
	v_dot2c_f32_f16_e32 v115, v72, v76
	v_dot2c_f32_f16_e32 v95, v66, v66
	v_dot2c_f32_f16_e32 v105, v37, v81
	v_dot2c_f32_f16_e32 v115, v73, v77
	v_dot2c_f32_f16_e32 v95, v67, v67
	s_waitcnt lgkmcnt(5)
	v_dot2c_f32_f16_e32 v105, v30, v82
	v_dot2c_f32_f16_e32 v115, v66, v78
	v_dot2c_f32_f16_e32 v95, v68, v68
	v_dot2c_f32_f16_e32 v105, v31, v83
	v_dot2c_f32_f16_e32 v115, v67, v79
	v_dot2c_f32_f16_e32 v95, v69, v69
	v_dot2c_f32_f16_e32 v105, v32, v84
	v_dot2c_f32_f16_e32 v115, v68, v80
	v_dot2c_f32_f16_e32 v95, v62, v62
	v_dot2c_f32_f16_e32 v105, v33, v85
	v_dot2c_f32_f16_e32 v115, v69, v81
	v_dot2c_f32_f16_e32 v95, v63, v63
	s_waitcnt lgkmcnt(4)
	v_dot2c_f32_f16_e32 v105, v26, v86
	v_dot2c_f32_f16_e32 v115, v62, v82
	v_dot2c_f32_f16_e32 v95, v64, v64
	v_dot2c_f32_f16_e32 v105, v27, v87
	v_dot2c_f32_f16_e32 v115, v63, v83
	v_dot2c_f32_f16_e32 v95, v65, v65
	v_dot2c_f32_f16_e32 v105, v28, v88
	v_dot2c_f32_f16_e32 v115, v64, v84
	v_dot2c_f32_f16_e32 v95, v58, v58
	v_dot2c_f32_f16_e32 v105, v29, v89
	v_dot2c_f32_f16_e32 v115, v65, v85
	v_dot2c_f32_f16_e32 v95, v59, v59
	s_waitcnt lgkmcnt(3)
	v_dot2c_f32_f16_e32 v105, v22, v90
	v_dot2c_f32_f16_e32 v115, v58, v86
	v_dot2c_f32_f16_e32 v95, v60, v60
	v_dot2c_f32_f16_e32 v105, v23, v91
	v_dot2c_f32_f16_e32 v115, v59, v87
	v_dot2c_f32_f16_e32 v95, v61, v61
	v_dot2c_f32_f16_e32 v105, v24, v92
	v_dot2c_f32_f16_e32 v115, v60, v88
	v_dot2c_f32_f16_e32 v95, v54, v54
	v_dot2c_f32_f16_e32 v105, v25, v93
	v_dot2c_f32_f16_e32 v115, v61, v89
	v_dot2c_f32_f16_e32 v95, v55, v55
	s_waitcnt lgkmcnt(2)
	v_dot2c_f32_f16_e32 v105, v18, v96
	v_dot2c_f32_f16_e32 v115, v54, v90
	v_dot2c_f32_f16_e32 v95, v56, v56
	v_dot2c_f32_f16_e32 v105, v19, v97
	v_dot2c_f32_f16_e32 v115, v55, v91
	v_dot2c_f32_f16_e32 v95, v57, v57
	v_dot2c_f32_f16_e32 v105, v20, v98
	v_dot2c_f32_f16_e32 v115, v56, v92
	v_dot2c_f32_f16_e32 v95, v50, v50
	v_dot2c_f32_f16_e32 v105, v21, v99
	v_dot2c_f32_f16_e32 v115, v57, v93
	v_dot2c_f32_f16_e32 v95, v51, v51
	s_waitcnt lgkmcnt(1)
	v_dot2c_f32_f16_e32 v105, v14, v100
	v_dot2c_f32_f16_e32 v115, v50, v96
	v_dot2c_f32_f16_e32 v95, v52, v52
	v_dot2c_f32_f16_e32 v105, v15, v101
	v_dot2c_f32_f16_e32 v115, v51, v97
	v_dot2c_f32_f16_e32 v95, v53, v53
	v_dot2c_f32_f16_e32 v105, v16, v102
	v_dot2c_f32_f16_e32 v115, v52, v98
	v_dot2c_f32_f16_e32 v95, v46, v46
	v_dot2c_f32_f16_e32 v105, v17, v103
	v_dot2c_f32_f16_e32 v115, v53, v99
	v_dot2c_f32_f16_e32 v95, v47, v47
	s_waitcnt lgkmcnt(0)
	v_dot2c_f32_f16_e32 v105, v10, v108
	v_dot2c_f32_f16_e32 v104, v12, v12
	v_dot2c_f32_f16_e32 v115, v46, v100
	v_dot2c_f32_f16_e32 v95, v48, v48
	v_dot2c_f32_f16_e32 v105, v11, v109
	v_dot2c_f32_f16_e32 v104, v13, v13
	v_dot2c_f32_f16_e32 v115, v47, v101
	v_dot2c_f32_f16_e32 v95, v49, v49
	v_dot2c_f32_f16_e32 v105, v12, v110
	v_dot2c_f32_f16_e32 v115, v48, v102
	v_dot2c_f32_f16_e32 v95, v42, v42
	v_mov_b32_e32 v74, v104
	v_dot2c_f32_f16_e32 v105, v13, v111
	v_dot2c_f32_f16_e32 v115, v49, v103
	v_dot2c_f32_f16_e32 v95, v43, v43
	v_permlane16_swap_b32_e32 v104, v74
	v_dot2c_f32_f16_e32 v115, v42, v108
	v_dot2c_f32_f16_e32 v95, v44, v44
	v_add_f32_e32 v133, v104, v74
	v_mov_b32_e32 v74, v105
	v_dot2c_f32_f16_e32 v115, v43, v109
	v_dot2c_f32_f16_e32 v95, v45, v45
	v_permlane16_swap_b32_e32 v105, v74
	v_dot2c_f32_f16_e32 v115, v44, v110
	v_add_f32_e32 v137, v105, v74
	v_mov_b32_e32 v74, v95
	v_dot2c_f32_f16_e32 v115, v45, v111
	s_nop 0
	v_permlane16_swap_b32_e32 v95, v74
	v_add_f32_e32 v135, v95, v74
	v_mov_b32_e32 v74, v115
	s_nop 1
	v_permlane16_swap_b32_e32 v115, v74
	v_add_f32_e32 v139, v115, v74
	v_lshlrev_b32_e32 v74, 8, v107
	v_lshlrev_b32_e32 v75, 3, v114
	s_movk_i32 s0, 0x78
	v_and_or_b32 v76, v75, s0, v74
	v_lshlrev_b32_e32 v75, 3, v141
	v_and_or_b32 v77, v75, s0, v74
	v_lshlrev_b32_e32 v75, 3, v142
	v_and_or_b32 v78, v75, s0, v74
	v_lshlrev_b32_e32 v75, 3, v143
	v_and_or_b32 v79, v75, s0, v74
	s_add_u32 s0, s26, 0x8000
	v_or_b32_e32 v108, 0x8000, v112
	v_mov_b32_e32 v123, 0
	s_addc_u32 s1, s27, 0
	v_readfirstlane_b32 s4, v108
	s_waitcnt vmcnt(0)
	s_barrier
	v_lshl_add_u64 v[74:75], s[0:1], 0, v[122:123]
	s_mov_b32 m0, s4
	s_nop 0
	global_load_lds_dwordx4 v[74:75], off
	s_addk_i32 s4, 0x400
	v_mov_b32_e32 v107, v123
	v_lshl_add_u64 v[74:75], s[0:1], 0, v[106:107]
	s_add_u32 s0, s26, 0xc000
	s_mov_b32 m0, s4
	s_nop 0
	global_load_lds_dwordx4 v[74:75], off
	s_addc_u32 s1, s27, 0
	v_or_b32_e32 v109, 0xc000, v112
	v_lshl_add_u64 v[74:75], s[0:1], 0, v[122:123]
	v_readfirstlane_b32 s4, v109
	s_mov_b32 m0, s4
	s_nop 0
	global_load_lds_dwordx4 v[74:75], off
	s_addk_i32 s4, 0x400
	v_lshl_add_u64 v[74:75], s[0:1], 0, v[106:107]
	s_mov_b32 m0, s4
	s_nop 0
	global_load_lds_dwordx4 v[74:75], off
	v_mov_b32_e32 v134, v133
	v_mov_b32_e32 v138, v137
	v_mov_b32_e32 v136, v135
	v_mov_b32_e32 v140, v139
	v_lshlrev_b32_e32 v144, 1, v76
	v_lshlrev_b32_e32 v143, 1, v77
	v_lshlrev_b32_e32 v142, 1, v78
	v_lshlrev_b32_e32 v141, 1, v79
	s_add_u32 s0, s26, 0x14000
	v_mov_b32_e32 v74, 0x7f61b1e6
	v_permlane32_swap_b32_e32 v133, v134
	v_permlane32_swap_b32_e32 v137, v138
	v_permlane32_swap_b32_e32 v135, v136
	v_permlane32_swap_b32_e32 v139, v140
	v_or_b32_e32 v160, 0x10000, v144
	v_or_b32_e32 v158, 0x10000, v143
	v_or_b32_e32 v156, 0x10000, v142
	v_or_b32_e32 v154, 0x10000, v141
	v_or_b32_e32 v159, 0x12000, v144
	v_or_b32_e32 v157, 0x12000, v143
	v_or_b32_e32 v155, 0x12000, v142
	v_or_b32_e32 v153, 0x12000, v141
	v_or_b32_e32 v152, 0x14000, v144
	v_or_b32_e32 v150, 0x14000, v143
	v_or_b32_e32 v148, 0x14000, v142
	v_or_b32_e32 v146, 0x14000, v141
	v_or_b32_e32 v151, 0x16000, v144
	v_or_b32_e32 v149, 0x16000, v143
	v_or_b32_e32 v147, 0x16000, v142
	v_or_b32_e32 v145, 0x16000, v141
	s_addc_u32 s1, s27, 0
	v_mov_b32_e32 v98, 0x7f800000
	s_mov_b32 s22, 0
	v_mov_b32_e32 v100, 0x7f800000
	v_mov_b32_e32 v99, 0x7f800000
	v_mov_b32_e32 v111, 0x7f800000
	v_mov_b32_e32 v101, 0x7f800000
	v_mov_b32_e32 v110, 0x7f800000
	v_mov_b32_e32 v75, v74
	v_mov_b32_e32 v76, v74
	v_mov_b32_e32 v77, v74
	v_mov_b32_e32 v78, v74
	v_mov_b32_e32 v79, v74
	v_mov_b32_e32 v80, v74
	v_mov_b32_e32 v81, v74
	v_mov_b32_e32 v82, v74
	v_mov_b32_e32 v83, v74
	v_mov_b32_e32 v84, v74
	v_mov_b32_e32 v85, v74
	v_mov_b32_e32 v86, v74
	v_mov_b32_e32 v87, v74
	v_mov_b32_e32 v88, v74
	v_mov_b32_e32 v89, v74
